# grid barrier: non-leader workgroups poll the top generation word directly (one release hop less); GQA leading-half epilogue partner reads issued 8/4/4 with counted waits; O-store tails of MLA and GQA
# speedup vs baseline: 1.0068x; 1.0068x over previous
; __device__ __forceinline__ unsigned xb_ld(unsigned* p)              { return __hip_atomic_load(p, __ATOMIC_RELAXED, __HIP_MEMORY_SCOPE_AGENT); }
; __device__ __forceinline__ unsigned xb_add(unsigned* p, unsigned v) { return __hip_atomic_fetch_add(p, v, __ATOMIC_RELAXED, __HIP_MEMORY_SCOPE_AGENT); }
; #define XB_SPIN(cond, bar) do { unsigned _sp = 0; while (cond) { __builtin_amdgcn_s_sleep(1); \
;     if ((++_sp & 255u) == 0u) { if (xb_ld(&(bar)[XB_TMO])) break; if (_sp > XB_SPIN_CAP) { atomicAdd(&(bar)[XB_TMO], 1u); break; } } } } while (0)
; __device__ __forceinline__ void xcd_barrier(const XcdBarrier& b) {
;     ...
;         const unsigned old = xb_add(&bar[XB_XSUB(b.x)], 1u);
;         const unsigned gen = old / nloc;
;         if (old + 1u == (gen + 1u) * nloc) {
;             __builtin_amdgcn_fence(__ATOMIC_RELEASE, "agent");
;             asm volatile("s_waitcnt vmcnt(0)" ::: "memory");
;             const unsigned og = xb_add(&bar[XB_TOP], 1u);
;             const unsigned tg = og / nx;
;             if (og + 1u == (tg + 1u) * nx) xb_add(&bar[XB_TOPGEN], 1u);
;             else XB_SPIN(xb_ld(&bar[XB_TOPGEN]) == tg, bar);
;             __builtin_amdgcn_fence(__ATOMIC_ACQUIRE, "agent");
;             xb_add(&bar[XB_XGEN(b.x)], 1u);
;             asm volatile("s_waitcnt vmcnt(0)" ::: "memory");
;         } else {
;             XB_SPIN(xb_ld(&bar[XB_XGEN(b.x)]) == gen, bar);
;             __builtin_amdgcn_fence(__ATOMIC_ACQUIRE, "agent");
;             asm volatile("s_waitcnt vmcnt(0)" ::: "memory");
;         }
.LBB0_129:
	s_or_b64 exec, exec, s[10:11]
	v_cvt_f32_u32_e32 v5, v3
	s_waitcnt vmcnt(0)
	v_readfirstlane_b32 s3, v4
	v_sub_u32_e32 v4, 0, v3
	v_rcp_iflag_f32_e32 v5, v5
	v_add_u32_e32 v6, s3, v2
	v_mul_f32_e32 v5, 0x4f7ffffe, v5
	v_cvt_u32_f32_e32 v5, v5
	v_mul_lo_u32 v2, v4, v5
	v_mul_hi_u32 v2, v5, v2
	v_add_u32_e32 v2, v5, v2
	v_mul_hi_u32 v2, v6, v2
	v_mul_lo_u32 v4, v2, v3
	v_sub_u32_e32 v4, v6, v4
	v_add_u32_e32 v5, 1, v2
	v_cmp_ge_u32_e32 vcc, v4, v3
	s_nop 1
	v_cndmask_b32_e32 v2, v2, v5, vcc
	v_sub_u32_e32 v5, v4, v3
	v_cndmask_b32_e32 v4, v4, v5, vcc
	v_add_u32_e32 v5, 1, v2
	v_cmp_ge_u32_e32 vcc, v4, v3
	v_add_u32_e32 v4, 1, v6
	s_nop 0
	v_cndmask_b32_e32 v2, v2, v5, vcc
	v_mul_lo_u32 v5, v3, v2
	v_add_u32_e32 v3, v5, v3
	v_cmp_ne_u32_e32 vcc, v4, v3
	s_and_saveexec_b64 s[8:9], vcc
	s_xor_b64 s[8:9], exec, s[8:9]
	s_cbranch_execz .LBB0_143
	s_waitcnt lgkmcnt(0)
	s_add_u32 s16, s84, 0x7500
	s_addc_u32 s17, s85, 0
	v_mov_b32_e32 v1, 0
	global_load_dword v1, v1, s[16:17] sc1
	s_waitcnt vmcnt(0)
	v_cmp_eq_u32_e32 vcc, v1, v2
	s_and_saveexec_b64 s[10:11], vcc
	s_cbranch_execz .LBB0_142
	s_add_u32 s14, s84, 0x4200
	s_addc_u32 s15, s85, 0
	s_mov_b32 s3, 1
	s_mov_b64 s[18:19], 0
	v_mov_b32_e32 v1, 0
	s_branch .LBB0_133

; __device__ __forceinline__ unsigned xb_ld(unsigned* p)              { return __hip_atomic_load(p, __ATOMIC_RELAXED, __HIP_MEMORY_SCOPE_AGENT); }
; __device__ __forceinline__ unsigned xb_add(unsigned* p, unsigned v) { return __hip_atomic_fetch_add(p, v, __ATOMIC_RELAXED, __HIP_MEMORY_SCOPE_AGENT); }
; #define XB_SPIN(cond, bar) do { unsigned _sp = 0; while (cond) { __builtin_amdgcn_s_sleep(1); \
;     if ((++_sp & 255u) == 0u) { if (xb_ld(&(bar)[XB_TMO])) break; if (_sp > XB_SPIN_CAP) { atomicAdd(&(bar)[XB_TMO], 1u); break; } } } } while (0)
; __device__ __forceinline__ void xcd_barrier(const XcdBarrier& b) {
;     ...
;         const unsigned old = xb_add(&bar[XB_XSUB(b.x)], 1u);
;         const unsigned gen = old / nloc;
;         if (old + 1u == (gen + 1u) * nloc) {
;             __builtin_amdgcn_fence(__ATOMIC_RELEASE, "agent");
;             asm volatile("s_waitcnt vmcnt(0)" ::: "memory");
;             const unsigned og = xb_add(&bar[XB_TOP], 1u);
;             const unsigned tg = og / nx;
;             if (og + 1u == (tg + 1u) * nx) xb_add(&bar[XB_TOPGEN], 1u);
;             else XB_SPIN(xb_ld(&bar[XB_TOPGEN]) == tg, bar);
;             __builtin_amdgcn_fence(__ATOMIC_ACQUIRE, "agent");
;             xb_add(&bar[XB_XGEN(b.x)], 1u);
;             asm volatile("s_waitcnt vmcnt(0)" ::: "memory");
;         } else {
;             XB_SPIN(xb_ld(&bar[XB_XGEN(b.x)]) == gen, bar);
;             __builtin_amdgcn_fence(__ATOMIC_ACQUIRE, "agent");
;             asm volatile("s_waitcnt vmcnt(0)" ::: "memory");
;         }
.LBB0_281:
	s_or_b64 exec, exec, s[10:11]
	v_cvt_f32_u32_e32 v5, v3
	s_waitcnt vmcnt(0)
	v_readfirstlane_b32 s3, v4
	v_sub_u32_e32 v4, 0, v3
	v_rcp_iflag_f32_e32 v5, v5
	v_add_u32_e32 v6, s3, v2
	v_mul_f32_e32 v5, 0x4f7ffffe, v5
	v_cvt_u32_f32_e32 v5, v5
	v_mul_lo_u32 v2, v4, v5
	v_mul_hi_u32 v2, v5, v2
	v_add_u32_e32 v2, v5, v2
	v_mul_hi_u32 v2, v6, v2
	v_mul_lo_u32 v4, v2, v3
	v_sub_u32_e32 v4, v6, v4
	v_add_u32_e32 v5, 1, v2
	v_cmp_ge_u32_e32 vcc, v4, v3
	s_nop 1
	v_cndmask_b32_e32 v2, v2, v5, vcc
	v_sub_u32_e32 v5, v4, v3
	v_cndmask_b32_e32 v4, v4, v5, vcc
	v_add_u32_e32 v5, 1, v2
	v_cmp_ge_u32_e32 vcc, v4, v3
	v_add_u32_e32 v4, 1, v6
	s_nop 0
	v_cndmask_b32_e32 v2, v2, v5, vcc
	v_mul_lo_u32 v5, v3, v2
	v_add_u32_e32 v3, v5, v3
	v_cmp_ne_u32_e32 vcc, v4, v3
	s_and_saveexec_b64 s[8:9], vcc
	s_xor_b64 s[8:9], exec, s[8:9]
	s_cbranch_execz .LBB0_295
	s_waitcnt lgkmcnt(0)
	s_add_u32 s16, s84, 0x7500
	s_addc_u32 s17, s85, 0
	v_mov_b32_e32 v1, 0
	global_load_dword v1, v1, s[16:17] sc1
	s_waitcnt vmcnt(0)
	v_cmp_eq_u32_e32 vcc, v1, v2
	s_and_saveexec_b64 s[10:11], vcc
	s_cbranch_execz .LBB0_294
	s_add_u32 s14, s84, 0x4200
	s_addc_u32 s15, s85, 0
	s_mov_b32 s3, 1
	s_mov_b64 s[18:19], 0
	s_branch .LBB0_285

; __device__ __forceinline__ unsigned xb_ld(unsigned* p)              { return __hip_atomic_load(p, __ATOMIC_RELAXED, __HIP_MEMORY_SCOPE_AGENT); }
; __device__ __forceinline__ unsigned xb_add(unsigned* p, unsigned v) { return __hip_atomic_fetch_add(p, v, __ATOMIC_RELAXED, __HIP_MEMORY_SCOPE_AGENT); }
; #define XB_SPIN(cond, bar) do { unsigned _sp = 0; while (cond) { __builtin_amdgcn_s_sleep(1); \
;     if ((++_sp & 255u) == 0u) { if (xb_ld(&(bar)[XB_TMO])) break; if (_sp > XB_SPIN_CAP) { atomicAdd(&(bar)[XB_TMO], 1u); break; } } } } while (0)
; __device__ __forceinline__ void xcd_barrier(const XcdBarrier& b) {
;     ...
;         const unsigned old = xb_add(&bar[XB_XSUB(b.x)], 1u);
;         const unsigned gen = old / nloc;
;         if (old + 1u == (gen + 1u) * nloc) {
;             __builtin_amdgcn_fence(__ATOMIC_RELEASE, "agent");
;             asm volatile("s_waitcnt vmcnt(0)" ::: "memory");
;             const unsigned og = xb_add(&bar[XB_TOP], 1u);
;             const unsigned tg = og / nx;
;             if (og + 1u == (tg + 1u) * nx) xb_add(&bar[XB_TOPGEN], 1u);
;             else XB_SPIN(xb_ld(&bar[XB_TOPGEN]) == tg, bar);
;             __builtin_amdgcn_fence(__ATOMIC_ACQUIRE, "agent");
;             xb_add(&bar[XB_XGEN(b.x)], 1u);
;             asm volatile("s_waitcnt vmcnt(0)" ::: "memory");
;         } else {
;             XB_SPIN(xb_ld(&bar[XB_XGEN(b.x)]) == gen, bar);
;             __builtin_amdgcn_fence(__ATOMIC_ACQUIRE, "agent");
;             asm volatile("s_waitcnt vmcnt(0)" ::: "memory");
;         }
.LBB0_351:
	s_or_b64 exec, exec, s[10:11]
	v_cvt_f32_u32_e32 v5, v3
	s_waitcnt vmcnt(0)
	v_readfirstlane_b32 s3, v4
	v_sub_u32_e32 v4, 0, v3
	v_rcp_iflag_f32_e32 v5, v5
	v_add_u32_e32 v6, s3, v1
	v_mul_f32_e32 v5, 0x4f7ffffe, v5
	v_cvt_u32_f32_e32 v5, v5
	v_mul_lo_u32 v1, v4, v5
	v_mul_hi_u32 v1, v5, v1
	v_add_u32_e32 v1, v5, v1
	v_mul_hi_u32 v1, v6, v1
	v_mul_lo_u32 v4, v1, v3
	v_sub_u32_e32 v4, v6, v4
	v_add_u32_e32 v5, 1, v1
	v_cmp_ge_u32_e32 vcc, v4, v3
	s_nop 1
	v_cndmask_b32_e32 v1, v1, v5, vcc
	v_sub_u32_e32 v5, v4, v3
	v_cndmask_b32_e32 v4, v4, v5, vcc
	v_add_u32_e32 v5, 1, v1
	v_cmp_ge_u32_e32 vcc, v4, v3
	v_add_u32_e32 v4, 1, v6
	s_nop 0
	v_cndmask_b32_e32 v1, v1, v5, vcc
	v_mul_lo_u32 v5, v3, v1
	v_add_u32_e32 v3, v5, v3
	v_cmp_ne_u32_e32 vcc, v4, v3
	s_and_saveexec_b64 s[8:9], vcc
	s_xor_b64 s[8:9], exec, s[8:9]
	s_cbranch_execz .LBB0_365
	s_waitcnt lgkmcnt(0)
	s_add_u32 s20, s34, 0x7500
	s_addc_u32 s21, s35, 0
	v_mov_b32_e32 v2, 0
	global_load_dword v2, v2, s[20:21] sc1
	s_waitcnt vmcnt(0)
	v_cmp_eq_u32_e32 vcc, v2, v1
	s_and_saveexec_b64 s[10:11], vcc
	s_cbranch_execz .LBB0_364
	s_add_u32 s14, s34, 0x4200
	s_addc_u32 s15, s35, 0
	s_mov_b32 s3, 1
	s_mov_b64 s[22:23], 0
	s_branch .LBB0_355

; __device__ __forceinline__ unsigned xb_ld(unsigned* p)              { return __hip_atomic_load(p, __ATOMIC_RELAXED, __HIP_MEMORY_SCOPE_AGENT); }
; __device__ __forceinline__ unsigned xb_add(unsigned* p, unsigned v) { return __hip_atomic_fetch_add(p, v, __ATOMIC_RELAXED, __HIP_MEMORY_SCOPE_AGENT); }
; #define XB_SPIN(cond, bar) do { unsigned _sp = 0; while (cond) { __builtin_amdgcn_s_sleep(1); \
;     if ((++_sp & 255u) == 0u) { if (xb_ld(&(bar)[XB_TMO])) break; if (_sp > XB_SPIN_CAP) { atomicAdd(&(bar)[XB_TMO], 1u); break; } } } } while (0)
; __device__ __forceinline__ void xcd_barrier(const XcdBarrier& b) {
;     ...
;         const unsigned old = xb_add(&bar[XB_XSUB(b.x)], 1u);
;         const unsigned gen = old / nloc;
;         if (old + 1u == (gen + 1u) * nloc) {
;             __builtin_amdgcn_fence(__ATOMIC_RELEASE, "agent");
;             asm volatile("s_waitcnt vmcnt(0)" ::: "memory");
;             const unsigned og = xb_add(&bar[XB_TOP], 1u);
;             const unsigned tg = og / nx;
;             if (og + 1u == (tg + 1u) * nx) xb_add(&bar[XB_TOPGEN], 1u);
;             else XB_SPIN(xb_ld(&bar[XB_TOPGEN]) == tg, bar);
;             __builtin_amdgcn_fence(__ATOMIC_ACQUIRE, "agent");
;             xb_add(&bar[XB_XGEN(b.x)], 1u);
;             asm volatile("s_waitcnt vmcnt(0)" ::: "memory");
;         } else {
;             XB_SPIN(xb_ld(&bar[XB_XGEN(b.x)]) == gen, bar);
;             __builtin_amdgcn_fence(__ATOMIC_ACQUIRE, "agent");
;             asm volatile("s_waitcnt vmcnt(0)" ::: "memory");
;         }
.LBB0_436:
	s_or_b64 exec, exec, s[10:11]
	v_cvt_f32_u32_e32 v6, v4
	s_waitcnt vmcnt(0)
	v_readfirstlane_b32 s8, v5
	v_sub_u32_e32 v5, 0, v4
	v_rcp_iflag_f32_e32 v6, v6
	v_add_u32_e32 v7, s8, v3
	v_mul_f32_e32 v6, 0x4f7ffffe, v6
	v_cvt_u32_f32_e32 v6, v6
	v_mul_lo_u32 v3, v5, v6
	v_mul_hi_u32 v3, v6, v3
	v_add_u32_e32 v3, v6, v3
	v_mul_hi_u32 v3, v7, v3
	v_mul_lo_u32 v5, v3, v4
	v_sub_u32_e32 v5, v7, v5
	v_add_u32_e32 v6, 1, v3
	v_cmp_ge_u32_e32 vcc, v5, v4
	s_nop 1
	v_cndmask_b32_e32 v3, v3, v6, vcc
	v_sub_u32_e32 v6, v5, v4
	v_cndmask_b32_e32 v5, v5, v6, vcc
	v_add_u32_e32 v6, 1, v3
	v_cmp_ge_u32_e32 vcc, v5, v4
	v_add_u32_e32 v5, 1, v7
	s_nop 0
	v_cndmask_b32_e32 v3, v3, v6, vcc
	v_mul_lo_u32 v6, v4, v3
	v_add_u32_e32 v4, v6, v4
	v_cmp_ne_u32_e32 vcc, v5, v4
	s_and_saveexec_b64 s[8:9], vcc
	s_xor_b64 s[8:9], exec, s[8:9]
	s_cbranch_execz .LBB0_450
	s_waitcnt lgkmcnt(0)
	s_add_u32 s22, s34, 0x7500
	s_addc_u32 s23, s35, 0
	v_mov_b32_e32 v2, 0
	global_load_dword v2, v2, s[22:23] sc1
	s_waitcnt vmcnt(0)
	v_cmp_eq_u32_e32 vcc, v2, v3
	s_and_saveexec_b64 s[10:11], vcc
	s_cbranch_execz .LBB0_449
	s_add_u32 s14, s34, 0x4200
	s_addc_u32 s15, s35, 0
	s_mov_b32 s16, 1
	s_mov_b64 s[26:27], 0
	s_branch .LBB0_440

; __device__ __forceinline__ unsigned xb_ld(unsigned* p)              { return __hip_atomic_load(p, __ATOMIC_RELAXED, __HIP_MEMORY_SCOPE_AGENT); }
; __device__ __forceinline__ unsigned xb_add(unsigned* p, unsigned v) { return __hip_atomic_fetch_add(p, v, __ATOMIC_RELAXED, __HIP_MEMORY_SCOPE_AGENT); }
; #define XB_SPIN(cond, bar) do { unsigned _sp = 0; while (cond) { __builtin_amdgcn_s_sleep(1); \
;     if ((++_sp & 255u) == 0u) { if (xb_ld(&(bar)[XB_TMO])) break; if (_sp > XB_SPIN_CAP) { atomicAdd(&(bar)[XB_TMO], 1u); break; } } } } while (0)
; __device__ __forceinline__ void xcd_barrier(const XcdBarrier& b) {
;     ...
;         const unsigned old = xb_add(&bar[XB_XSUB(b.x)], 1u);
;         const unsigned gen = old / nloc;
;         if (old + 1u == (gen + 1u) * nloc) {
;             __builtin_amdgcn_fence(__ATOMIC_RELEASE, "agent");
;             asm volatile("s_waitcnt vmcnt(0)" ::: "memory");
;             const unsigned og = xb_add(&bar[XB_TOP], 1u);
;             const unsigned tg = og / nx;
;             if (og + 1u == (tg + 1u) * nx) xb_add(&bar[XB_TOPGEN], 1u);
;             else XB_SPIN(xb_ld(&bar[XB_TOPGEN]) == tg, bar);
;             __builtin_amdgcn_fence(__ATOMIC_ACQUIRE, "agent");
;             xb_add(&bar[XB_XGEN(b.x)], 1u);
;             asm volatile("s_waitcnt vmcnt(0)" ::: "memory");
;         } else {
;             XB_SPIN(xb_ld(&bar[XB_XGEN(b.x)]) == gen, bar);
;             __builtin_amdgcn_fence(__ATOMIC_ACQUIRE, "agent");
;             asm volatile("s_waitcnt vmcnt(0)" ::: "memory");
;         }
.LBB0_540:
	s_or_b64 exec, exec, s[24:25]
	v_cvt_f32_u32_e32 v6, v4
	s_waitcnt vmcnt(0)
	v_readfirstlane_b32 s14, v5
	v_sub_u32_e32 v5, 0, v4
	v_rcp_iflag_f32_e32 v6, v6
	v_add_u32_e32 v7, s14, v3
	v_mul_f32_e32 v6, 0x4f7ffffe, v6
	v_cvt_u32_f32_e32 v6, v6
	v_mul_lo_u32 v3, v5, v6
	v_mul_hi_u32 v3, v6, v3
	v_add_u32_e32 v3, v6, v3
	v_mul_hi_u32 v3, v7, v3
	v_mul_lo_u32 v5, v3, v4
	v_sub_u32_e32 v5, v7, v5
	v_add_u32_e32 v6, 1, v3
	v_cmp_ge_u32_e32 vcc, v5, v4
	s_nop 1
	v_cndmask_b32_e32 v3, v3, v6, vcc
	v_sub_u32_e32 v6, v5, v4
	v_cndmask_b32_e32 v5, v5, v6, vcc
	v_add_u32_e32 v6, 1, v3
	v_cmp_ge_u32_e32 vcc, v5, v4
	v_add_u32_e32 v5, 1, v7
	s_nop 0
	v_cndmask_b32_e32 v3, v3, v6, vcc
	v_mul_lo_u32 v6, v4, v3
	v_add_u32_e32 v4, v6, v4
	v_cmp_ne_u32_e32 vcc, v5, v4
	s_and_saveexec_b64 s[14:15], vcc
	s_xor_b64 s[14:15], exec, s[14:15]
	s_cbranch_execz .LBB0_554
	s_waitcnt lgkmcnt(0)
	s_add_u32 s36, s34, 0x7500
	s_addc_u32 s37, s35, 0
	v_mov_b32_e32 v2, 0
	global_load_dword v2, v2, s[36:37] sc1
	s_waitcnt vmcnt(0)
	v_cmp_eq_u32_e32 vcc, v2, v3
	s_and_saveexec_b64 s[28:29], vcc
	s_cbranch_execz .LBB0_553
	s_add_u32 s30, s34, 0x4200
	s_addc_u32 s31, s35, 0
	s_mov_b32 s16, 1
	s_mov_b64 s[40:41], 0
	s_branch .LBB0_544

; #define LAS __attribute__((address_space(3)))
; __device__ __forceinline__ unsigned cvtpk(float lo, float hi) { f32x2 v = {lo, hi}; bf16x2_t b = __builtin_convertvector(v, bf16x2_t); return __builtin_bit_cast(unsigned, b); }
; #define ATT_SB() __builtin_amdgcn_sched_barrier(0)
; #define ATT_VLOAD(sl, h_) do { _Pragma("unroll") for (int g_ = 0; g_ < NVF; ++g_) { \
;         if constexpr (KS) vf[g_] = *(const LAS bf16x8*)(vpk + (sl) * VSLOT + g_ * 2048); \
;         else vf[g_] = *(const LAS bf16x8*)(vp[g_ & 1] + (sl) * VSLOT + ((h_) * 4 + (g_ >> 1)) * 2048); } } while (0)
; template <int DQK, int DV, bool LEAD> ...
;     ...
;     ATT_VLOAD(s_prev, 0); ATT_PVP(0);
;     if constexpr (DV == 128) { ATT_SB(); ATT_VLOAD(s_prev, 1); ATT_PVP(1); }
; #pragma unroll
;     for (int qb = 0; qb < NQB; ++qb) lsum[qb] = lanes4_sum(lsum[qb]);
;     if constexpr (KS) {
;         wait_bar<0>();
;         LAS unsigned char* xch = shm + (wid & 3) * 17408;
;         if constexpr (!LEAD) {
; #pragma unroll
;             for (int db = 0; db < 4; ++db)
; #pragma unroll
;                 for (int qb = 0; qb < 4; ++qb) *(LAS f32x4*)(xch + ((db * 4 + qb) * 64 + lane) * 16) = o[db][qb];
; #pragma unroll
;             for (int qb = 0; qb < 4; ++qb) *(LAS float*)(xch + 16384 + (qb * 64 + lane) * 4) = lsum[qb];
;         }
;         asm volatile("s_waitcnt lgkmcnt(0)\n\ts_barrier" ::: "memory");
;         if constexpr (LEAD) {
;             float inv[4];
; #pragma unroll
;             for (int qb = 0; qb < 4; ++qb) inv[qb] = 1.0f / (lsum[qb] + *(const LAS float*)(xch + 16384 + (qb * 64 + lane) * 4));
;             LAS unsigned char* stg = shm + ATT_LDS + (wid & 3) * 8192;
; #pragma unroll
;             for (int dbl = 0; dbl < 4; ++dbl)
; #pragma unroll
;                 for (int qb = 0; qb < 4; ++qb) { const f32x4 ov = o[dbl][qb] + *(const LAS f32x4*)(xch + ((dbl * 4 + qb) * 64 + lane) * 16); const int row = qb * 16 + q16;
;                     u32x2 w; w.x = cvtpk(ov[0] * inv[qb], ov[1] * inv[qb]); w.y = cvtpk(ov[2] * inv[qb], ov[3] * inv[qb]);
;                     *(LAS u32x2*)(stg + row * 128 + (((4 * dbl + g4) ^ ((row & 7) << 1)) << 3)) = w; }
.LBB0_639:
	v_lshl_add_u32 v14, s31, 13, v210
	ds_read_b128 v[2:5], v14 offset:36864
	ds_read_b128 v[6:9], v14 offset:38912
	ds_read_b128 v[10:13], v14 offset:40960
	s_waitcnt lgkmcnt(4)
	ds_read_b128 v[66:69], v14 offset:43008
	s_lshl_b32 s4, s6, 1
	s_waitcnt lgkmcnt(3)
	v_mfma_f32_16x16x32_bf16 v[62:65], v[2:5], v[138:141], v[134:137]
	s_add_u32 s4, s14, s4
	s_mul_i32 s6, s30, 0x4400
	s_addc_u32 s5, s15, 0
	v_mfma_f32_16x16x32_bf16 v[58:61], v[2:5], v[142:145], v[130:133]
	s_waitcnt vmcnt(0) lgkmcnt(0)
	s_barrier
	s_add_i32 s7, s6, 0
	s_waitcnt lgkmcnt(0)
	s_barrier
	v_mfma_f32_16x16x32_bf16 v[54:57], v[2:5], v[146:149], v[126:129]
	v_lshl_add_u32 v70, v218, 2, s7
	s_lshl_b32 s6, s30, 13
	s_add_i32 s6, s6, 0
	v_mfma_f32_16x16x32_bf16 v[50:53], v[2:5], v[150:153], v[122:125]
	s_add_i32 s6, s6, 0x15000
	s_waitcnt lgkmcnt(2)
	v_mfma_f32_16x16x32_bf16 v[46:49], v[6:9], v[138:141], v[118:121]
	v_mfma_f32_16x16x32_bf16 v[42:45], v[6:9], v[142:145], v[114:117]
	v_mfma_f32_16x16x32_bf16 v[38:41], v[6:9], v[146:149], v[110:113]
	v_mfma_f32_16x16x32_bf16 v[34:37], v[6:9], v[150:153], v[106:109]
	s_waitcnt lgkmcnt(1)
	v_mfma_f32_16x16x32_bf16 v[30:33], v[10:13], v[138:141], v[102:105]
	v_mfma_f32_16x16x32_bf16 v[26:29], v[10:13], v[142:145], v[98:101]
	v_mfma_f32_16x16x32_bf16 v[22:25], v[10:13], v[146:149], v[94:97]
	v_mfma_f32_16x16x32_bf16 v[18:21], v[10:13], v[150:153], v[90:93]
	s_waitcnt lgkmcnt(0)
	v_mfma_f32_16x16x32_bf16 v[14:17], v[66:69], v[138:141], v[86:89]
	v_mfma_f32_16x16x32_bf16 v[10:13], v[66:69], v[142:145], v[82:85]
	v_mfma_f32_16x16x32_bf16 v[6:9], v[66:69], v[146:149], v[78:81]
	v_mfma_f32_16x16x32_bf16 v[2:5], v[66:69], v[150:153], v[74:77]
	v_mov_b32_e32 v66, v205
	s_nop 1
	v_permlane16_swap_b32_e32 v205, v66
	v_add_f32_e32 v66, v205, v66
	v_mov_b32_e32 v67, v66
	s_nop 1
	v_permlane32_swap_b32_e32 v66, v67
	v_add_f32_e32 v68, v66, v67
	v_mov_b32_e32 v66, v204
	s_nop 1
	v_permlane16_swap_b32_e32 v204, v66
	v_add_f32_e32 v66, v204, v66
	v_mov_b32_e32 v67, v66
	s_nop 1
	v_permlane32_swap_b32_e32 v66, v67
	v_add_f32_e32 v69, v66, v67
	v_mov_b32_e32 v66, v193
	s_nop 1
	v_permlane16_swap_b32_e32 v193, v66
	v_add_f32_e32 v66, v193, v66
	v_mov_b32_e32 v67, v66
	s_nop 1
	v_permlane32_swap_b32_e32 v66, v67
	v_add_f32_e32 v72, v66, v67
	v_mov_b32_e32 v66, v192
	s_nop 1
	v_permlane16_swap_b32_e32 v192, v66
	v_add_f32_e32 v66, v192, v66
	v_mov_b32_e32 v67, v66
	s_nop 1
	v_permlane32_swap_b32_e32 v66, v67
	v_add_f32_e32 v73, v66, v67
	ds_read2st64_b32 v[66:67], v70 offset0:64 offset1:65
	s_waitcnt lgkmcnt(0)
	v_add_f32_e32 v66, v68, v66
	v_div_scale_f32 v68, s[40:41], v66, v66, 1.0
	v_rcp_f32_e32 v71, v68
	s_nop 0
	v_fma_f32 v74, -v68, v71, 1.0
	v_fmac_f32_e32 v71, v74, v71
	v_div_scale_f32 v74, vcc, 1.0, v66, 1.0
	v_mul_f32_e32 v75, v74, v71
	v_fma_f32 v76, -v68, v75, v74
	v_fmac_f32_e32 v75, v76, v71
	v_fma_f32 v68, -v68, v75, v74
	v_div_fmas_f32 v68, v68, v71, v75
	v_div_fixup_f32 v68, v68, v66, 1.0
	v_add_f32_e32 v66, v69, v67
	v_div_scale_f32 v67, s[40:41], v66, v66, 1.0
	v_rcp_f32_e32 v69, v67
	s_nop 0
	v_fma_f32 v71, -v67, v69, 1.0
	v_fmac_f32_e32 v69, v71, v69
	v_div_scale_f32 v71, vcc, 1.0, v66, 1.0
	v_mul_f32_e32 v74, v71, v69
	v_fma_f32 v75, -v67, v74, v71
	v_fmac_f32_e32 v74, v75, v69
	v_fma_f32 v67, -v67, v74, v71
	ds_read2st64_b32 v[70:71], v70 offset0:66 offset1:67
	v_div_fmas_f32 v67, v67, v69, v74
	v_div_fixup_f32 v66, v67, v66, 1.0
	s_waitcnt lgkmcnt(0)
	v_add_f32_e32 v67, v72, v70
	v_div_scale_f32 v69, s[40:41], v67, v67, 1.0
	v_rcp_f32_e32 v70, v69
	s_nop 0
	v_fma_f32 v72, -v69, v70, 1.0
	v_fmac_f32_e32 v70, v72, v70
	v_div_scale_f32 v72, vcc, 1.0, v67, 1.0
	v_mul_f32_e32 v74, v72, v70
	v_fma_f32 v75, -v69, v74, v72
	v_fmac_f32_e32 v74, v75, v70
	v_fma_f32 v69, -v69, v74, v72
	v_div_fmas_f32 v69, v69, v70, v74
	v_div_fixup_f32 v72, v69, v67, 1.0
	v_add_f32_e32 v67, v73, v71
	v_div_scale_f32 v69, s[40:41], v67, v67, 1.0
	v_rcp_f32_e32 v70, v69
	s_nop 0
	v_fma_f32 v71, -v69, v70, 1.0
	v_fmac_f32_e32 v70, v71, v70
	v_div_scale_f32 v71, vcc, 1.0, v67, 1.0
	v_mul_f32_e32 v73, v71, v70
	v_fma_f32 v74, -v69, v73, v71
	v_fmac_f32_e32 v73, v74, v70
	v_fma_f32 v69, -v69, v73, v71
	v_div_fmas_f32 v69, v69, v70, v73
	v_div_fixup_f32 v70, v69, v67, 1.0
	v_lshl_add_u32 v67, v218, 4, s7
	ds_read_b128 v[154:157], v67
	ds_read_b128 v[158:161], v67 offset:1024
	ds_read_b128 v[162:165], v67 offset:2048
	ds_read_b128 v[166:169], v67 offset:3072
	ds_read_b128 v[170:173], v67 offset:4096
	ds_read_b128 v[174:177], v67 offset:5120
	ds_read_b128 v[178:181], v67 offset:6144
	ds_read_b128 v[182:185], v67 offset:7168
	v_add_u32_e32 v69, s6, v207
	v_bitop3_b32 v73, v194, v217, 14 bitop3:0x78
	v_lshl_add_u32 v73, v73, 3, v69
	v_and_b32_e32 v71, 14, v217
	s_waitcnt lgkmcnt(4)
	v_pk_add_f32 v[62:63], v[62:63], v[154:155]
	v_pk_add_f32 v[64:65], v[64:65], v[156:157]
	v_pk_mul_f32 v[62:63], v[68:69], v[62:63] op_sel_hi:[0,1]
	v_cvt_pk_bf16_f32 v74, v62, v63
	v_pk_mul_f32 v[62:63], v[68:69], v[64:65] op_sel_hi:[0,1]
	v_cvt_pk_bf16_f32 v75, v62, v63
	v_pk_add_f32 v[60:61], v[60:61], v[160:161]
	v_pk_add_f32 v[58:59], v[58:59], v[158:159]
	v_pk_mul_f32 v[60:61], v[66:67], v[60:61] op_sel_hi:[0,1]
	v_pk_mul_f32 v[58:59], v[66:67], v[58:59] op_sel_hi:[0,1]
	v_cvt_pk_bf16_f32 v58, v58, v59
	v_cvt_pk_bf16_f32 v59, v60, v61
	ds_write2st64_b64 v73, v[74:75], v[58:59] offset1:4
	v_pk_add_f32 v[54:55], v[54:55], v[162:163]
	v_pk_add_f32 v[56:57], v[56:57], v[164:165]
	v_pk_mul_f32 v[54:55], v[72:73], v[54:55] op_sel_hi:[0,1]
	v_cvt_pk_bf16_f32 v58, v54, v55
	v_pk_mul_f32 v[54:55], v[72:73], v[56:57] op_sel_hi:[0,1]
	v_cvt_pk_bf16_f32 v59, v54, v55
	v_pk_add_f32 v[52:53], v[52:53], v[168:169]
	v_pk_add_f32 v[50:51], v[50:51], v[166:167]
	v_pk_mul_f32 v[52:53], v[70:71], v[52:53] op_sel_hi:[0,1]
	v_pk_mul_f32 v[50:51], v[70:71], v[50:51] op_sel_hi:[0,1]
	v_cvt_pk_bf16_f32 v50, v50, v51
	v_cvt_pk_bf16_f32 v51, v52, v53
	ds_write2st64_b64 v73, v[58:59], v[50:51] offset0:8 offset1:12
	v_bitop3_b32 v50, v206, v217, 14 bitop3:0x78
	v_lshl_add_u32 v54, v50, 3, v69
	ds_read_b128 v[154:157], v67 offset:8192
	ds_read_b128 v[158:161], v67 offset:9216
	ds_read_b128 v[162:165], v67 offset:10240
	ds_read_b128 v[166:169], v67 offset:11264
	s_waitcnt lgkmcnt(6)
; #define LAS __attribute__((address_space(3)))
; __device__ __forceinline__ unsigned cvtpk(float lo, float hi) { f32x2 v = {lo, hi}; bf16x2_t b = __builtin_convertvector(v, bf16x2_t); return __builtin_bit_cast(unsigned, b); }
; template <int DQK, int DV, bool LEAD> ...
;     ...
;             for (int dbl = 0; dbl < 4; ++dbl)
; #pragma unroll
;                 for (int qb = 0; qb < 4; ++qb) { const f32x4 ov = o[dbl][qb] + *(const LAS f32x4*)(xch + ((dbl * 4 + qb) * 64 + lane) * 16); const int row = qb * 16 + q16;
;                     u32x2 w; w.x = cvtpk(ov[0] * inv[qb], ov[1] * inv[qb]); w.y = cvtpk(ov[2] * inv[qb], ov[3] * inv[qb]);
;                     *(LAS u32x2*)(stg + row * 128 + (((4 * dbl + g4) ^ ((row & 7) << 1)) << 3)) = w; }
;             asm volatile("s_waitcnt lgkmcnt(0)" ::: "memory");
; #pragma unroll
;             for (int rr = 0; rr < 8; ++rr) { const int row = rr * 8 + (lane >> 3), ch = lane & 7;
;                 const u32x4 v = *(const LAS u32x4*)(stg + row * 128 + ((ch ^ (row & 7)) << 4));
;                 *(u32x4*)(O + (size_t)(qrow0 + qoff + row) * opitch + ch * 8) = v; }
;             asm volatile("s_waitcnt lgkmcnt(0)" ::: "memory");
	v_pk_add_f32 v[46:47], v[46:47], v[170:171]
	v_pk_add_f32 v[48:49], v[48:49], v[172:173]
	v_pk_mul_f32 v[46:47], v[68:69], v[46:47] op_sel_hi:[0,1]
	v_cvt_pk_bf16_f32 v50, v46, v47
	v_pk_mul_f32 v[46:47], v[68:69], v[48:49] op_sel_hi:[0,1]
	v_cvt_pk_bf16_f32 v51, v46, v47
	v_pk_add_f32 v[44:45], v[44:45], v[176:177]
	v_pk_add_f32 v[42:43], v[42:43], v[174:175]
	v_pk_mul_f32 v[44:45], v[66:67], v[44:45] op_sel_hi:[0,1]
	v_pk_mul_f32 v[42:43], v[66:67], v[42:43] op_sel_hi:[0,1]
	v_cvt_pk_bf16_f32 v42, v42, v43
	v_cvt_pk_bf16_f32 v43, v44, v45
	ds_write2st64_b64 v54, v[50:51], v[42:43] offset1:4
	v_pk_add_f32 v[38:39], v[38:39], v[178:179]
	v_pk_add_f32 v[40:41], v[40:41], v[180:181]
	v_pk_mul_f32 v[38:39], v[72:73], v[38:39] op_sel_hi:[0,1]
	v_cvt_pk_bf16_f32 v42, v38, v39
	v_pk_mul_f32 v[38:39], v[72:73], v[40:41] op_sel_hi:[0,1]
	v_cvt_pk_bf16_f32 v43, v38, v39
	v_pk_add_f32 v[36:37], v[36:37], v[184:185]
	v_pk_add_f32 v[34:35], v[34:35], v[182:183]
	v_pk_mul_f32 v[36:37], v[70:71], v[36:37] op_sel_hi:[0,1]
	v_pk_mul_f32 v[34:35], v[70:71], v[34:35] op_sel_hi:[0,1]
	v_cvt_pk_bf16_f32 v34, v34, v35
	v_cvt_pk_bf16_f32 v35, v36, v37
	ds_write2st64_b64 v54, v[42:43], v[34:35] offset0:8 offset1:12
	v_bitop3_b32 v34, v194, v71, 8 bitop3:0x36
	v_lshl_add_u32 v38, v34, 3, v69
	ds_read_b128 v[170:173], v67 offset:12288
	ds_read_b128 v[174:177], v67 offset:13312
	ds_read_b128 v[178:181], v67 offset:14336
	ds_read_b128 v[182:185], v67 offset:15360
	s_waitcnt lgkmcnt(6)
	v_pk_add_f32 v[30:31], v[30:31], v[154:155]
	v_pk_add_f32 v[32:33], v[32:33], v[156:157]
	v_pk_mul_f32 v[30:31], v[68:69], v[30:31] op_sel_hi:[0,1]
	v_cvt_pk_bf16_f32 v34, v30, v31
	v_pk_mul_f32 v[30:31], v[68:69], v[32:33] op_sel_hi:[0,1]
	v_cvt_pk_bf16_f32 v35, v30, v31
	v_pk_add_f32 v[28:29], v[28:29], v[160:161]
	v_pk_add_f32 v[26:27], v[26:27], v[158:159]
	v_pk_mul_f32 v[28:29], v[66:67], v[28:29] op_sel_hi:[0,1]
	v_pk_mul_f32 v[26:27], v[66:67], v[26:27] op_sel_hi:[0,1]
	v_cvt_pk_bf16_f32 v26, v26, v27
	v_cvt_pk_bf16_f32 v27, v28, v29
	ds_write2st64_b64 v38, v[34:35], v[26:27] offset1:4
	v_pk_add_f32 v[22:23], v[22:23], v[162:163]
	v_pk_add_f32 v[24:25], v[24:25], v[164:165]
	v_pk_mul_f32 v[22:23], v[72:73], v[22:23] op_sel_hi:[0,1]
	v_cvt_pk_bf16_f32 v26, v22, v23
	v_pk_mul_f32 v[22:23], v[72:73], v[24:25] op_sel_hi:[0,1]
	v_cvt_pk_bf16_f32 v27, v22, v23
	v_pk_add_f32 v[20:21], v[20:21], v[168:169]
	v_pk_add_f32 v[18:19], v[18:19], v[166:167]
	v_pk_mul_f32 v[20:21], v[70:71], v[20:21] op_sel_hi:[0,1]
	v_pk_mul_f32 v[18:19], v[70:71], v[18:19] op_sel_hi:[0,1]
	v_cvt_pk_bf16_f32 v18, v18, v19
	v_cvt_pk_bf16_f32 v19, v20, v21
	ds_write2st64_b64 v38, v[26:27], v[18:19] offset0:8 offset1:12
	v_bitop3_b32 v18, v194, v71, 12 bitop3:0x36
	v_lshl_add_u32 v22, v18, 3, v69
	v_lshlrev_b32_e32 v194, 4, v216
	s_waitcnt lgkmcnt(2)
	v_pk_add_f32 v[14:15], v[14:15], v[170:171]
	v_pk_add_f32 v[16:17], v[16:17], v[172:173]
	v_pk_mul_f32 v[14:15], v[68:69], v[14:15] op_sel_hi:[0,1]
	v_cvt_pk_bf16_f32 v18, v14, v15
	v_pk_mul_f32 v[14:15], v[68:69], v[16:17] op_sel_hi:[0,1]
	v_cvt_pk_bf16_f32 v19, v14, v15
	v_pk_add_f32 v[12:13], v[12:13], v[176:177]
	v_pk_add_f32 v[10:11], v[10:11], v[174:175]
	v_pk_mul_f32 v[12:13], v[66:67], v[12:13] op_sel_hi:[0,1]
	v_pk_mul_f32 v[10:11], v[66:67], v[10:11] op_sel_hi:[0,1]
	v_cvt_pk_bf16_f32 v10, v10, v11
	v_cvt_pk_bf16_f32 v11, v12, v13
	ds_write2st64_b64 v22, v[18:19], v[10:11] offset1:4
	v_pk_add_f32 v[6:7], v[6:7], v[178:179]
	v_pk_add_f32 v[8:9], v[8:9], v[180:181]
	v_pk_mul_f32 v[6:7], v[72:73], v[6:7] op_sel_hi:[0,1]
	v_cvt_pk_bf16_f32 v10, v6, v7
	v_pk_mul_f32 v[6:7], v[72:73], v[8:9] op_sel_hi:[0,1]
	v_cvt_pk_bf16_f32 v11, v6, v7
	v_pk_add_f32 v[4:5], v[4:5], v[184:185]
	v_pk_add_f32 v[2:3], v[2:3], v[182:183]
	v_pk_mul_f32 v[4:5], v[70:71], v[4:5] op_sel_hi:[0,1]
	v_pk_mul_f32 v[2:3], v[70:71], v[2:3] op_sel_hi:[0,1]
	v_cvt_pk_bf16_f32 v2, v2, v3
	v_cvt_pk_bf16_f32 v3, v4, v5
	ds_write2st64_b64 v22, v[10:11], v[2:3] offset0:8 offset1:12
	v_xor_b32_e32 v2, v203, v216
	v_lshl_add_u32 v10, v2, 4, s6
	s_waitcnt lgkmcnt(0)
	v_lshl_add_u32 v2, v203, 7, v10
	ds_read_b128 v[154:157], v2
	v_or_b32_e32 v8, 8, v203
	v_lshl_add_u32 v2, v8, 7, v10
	ds_read_b128 v[158:161], v2
	v_or_b32_e32 v8, 16, v203
	v_lshl_add_u32 v2, v8, 7, v10
	ds_read_b128 v[162:165], v2
	v_or_b32_e32 v8, 24, v203
	v_lshl_add_u32 v2, v8, 7, v10
	ds_read_b128 v[166:169], v2
	v_or_b32_e32 v8, 32, v203
	v_lshl_add_u32 v2, v8, 7, v10
	ds_read_b128 v[170:173], v2
	v_or_b32_e32 v8, 40, v203
	v_lshl_add_u32 v2, v8, 7, v10
	ds_read_b128 v[174:177], v2
	v_or_b32_e32 v8, 48, v203
	v_lshl_add_u32 v2, v8, 7, v10
	ds_read_b128 v[178:181], v2
	v_or_b32_e32 v8, 56, v203
	v_lshl_add_u32 v2, v8, 7, v10
	ds_read_b128 v[182:185], v2
	v_lshl_add_u64 v[6:7], s[4:5], 0, v[194:195]
	v_or_b32_e32 v8, s25, v203
	v_ashrrev_i32_e32 v9, 31, v8
	v_lshlrev_b64 v[8:9], 11, v[8:9]
	v_lshl_add_u64 v[8:9], v[6:7], 0, v[8:9]
	s_waitcnt lgkmcnt(7)
	global_store_dwordx4 v[8:9], v[154:157], off
	v_or_b32_e32 v8, 8, v203
	v_or_b32_e32 v8, s25, v8
	v_ashrrev_i32_e32 v9, 31, v8
	v_lshlrev_b64 v[8:9], 11, v[8:9]
	v_lshl_add_u64 v[8:9], v[6:7], 0, v[8:9]
	s_waitcnt lgkmcnt(6)
	global_store_dwordx4 v[8:9], v[158:161], off
	v_or_b32_e32 v8, 16, v203
	v_or_b32_e32 v8, s25, v8
	v_ashrrev_i32_e32 v9, 31, v8
	v_lshlrev_b64 v[8:9], 11, v[8:9]
	v_lshl_add_u64 v[8:9], v[6:7], 0, v[8:9]
	s_waitcnt lgkmcnt(5)
	global_store_dwordx4 v[8:9], v[162:165], off
	v_or_b32_e32 v8, 24, v203
	v_or_b32_e32 v8, s25, v8
	v_ashrrev_i32_e32 v9, 31, v8
	v_lshlrev_b64 v[8:9], 11, v[8:9]
	v_lshl_add_u64 v[8:9], v[6:7], 0, v[8:9]
	s_waitcnt lgkmcnt(4)
	global_store_dwordx4 v[8:9], v[166:169], off
	v_or_b32_e32 v8, 32, v203
	v_or_b32_e32 v8, s25, v8
	v_ashrrev_i32_e32 v9, 31, v8
	v_lshlrev_b64 v[8:9], 11, v[8:9]
	v_lshl_add_u64 v[8:9], v[6:7], 0, v[8:9]
	s_waitcnt lgkmcnt(3)
	global_store_dwordx4 v[8:9], v[170:173], off
	v_or_b32_e32 v8, 40, v203
	v_or_b32_e32 v8, s25, v8
	v_ashrrev_i32_e32 v9, 31, v8
	v_lshlrev_b64 v[8:9], 11, v[8:9]
	v_lshl_add_u64 v[8:9], v[6:7], 0, v[8:9]
	s_waitcnt lgkmcnt(2)
	global_store_dwordx4 v[8:9], v[174:177], off
	v_or_b32_e32 v8, 48, v203
	v_or_b32_e32 v8, s25, v8
	v_ashrrev_i32_e32 v9, 31, v8
	v_lshlrev_b64 v[8:9], 11, v[8:9]
	v_lshl_add_u64 v[8:9], v[6:7], 0, v[8:9]
	s_waitcnt lgkmcnt(1)
	global_store_dwordx4 v[8:9], v[178:181], off
	v_or_b32_e32 v8, 56, v203
	v_or_b32_e32 v8, s25, v8
	v_ashrrev_i32_e32 v9, 31, v8
	v_lshlrev_b64 v[8:9], 11, v[8:9]
	v_lshl_add_u64 v[8:9], v[6:7], 0, v[8:9]
	s_waitcnt lgkmcnt(0)
	global_store_dwordx4 v[8:9], v[182:185], off
	s_waitcnt lgkmcnt(0)
	s_waitcnt lgkmcnt(0)
	s_barrier

; __device__ __forceinline__ unsigned xb_ld(unsigned* p)              { return __hip_atomic_load(p, __ATOMIC_RELAXED, __HIP_MEMORY_SCOPE_AGENT); }
; __device__ __forceinline__ unsigned xb_add(unsigned* p, unsigned v) { return __hip_atomic_fetch_add(p, v, __ATOMIC_RELAXED, __HIP_MEMORY_SCOPE_AGENT); }
; #define XB_SPIN(cond, bar) do { unsigned _sp = 0; while (cond) { __builtin_amdgcn_s_sleep(1); \
;     if ((++_sp & 255u) == 0u) { if (xb_ld(&(bar)[XB_TMO])) break; if (_sp > XB_SPIN_CAP) { atomicAdd(&(bar)[XB_TMO], 1u); break; } } } } while (0)
; __device__ __forceinline__ void xcd_barrier(const XcdBarrier& b) {
;     ...
;         const unsigned old = xb_add(&bar[XB_XSUB(b.x)], 1u);
;         const unsigned gen = old / nloc;
;         if (old + 1u == (gen + 1u) * nloc) {
;             __builtin_amdgcn_fence(__ATOMIC_RELEASE, "agent");
;             asm volatile("s_waitcnt vmcnt(0)" ::: "memory");
;             const unsigned og = xb_add(&bar[XB_TOP], 1u);
;             const unsigned tg = og / nx;
;             if (og + 1u == (tg + 1u) * nx) xb_add(&bar[XB_TOPGEN], 1u);
;             else XB_SPIN(xb_ld(&bar[XB_TOPGEN]) == tg, bar);
;             __builtin_amdgcn_fence(__ATOMIC_ACQUIRE, "agent");
;             xb_add(&bar[XB_XGEN(b.x)], 1u);
;             asm volatile("s_waitcnt vmcnt(0)" ::: "memory");
;         } else {
;             XB_SPIN(xb_ld(&bar[XB_XGEN(b.x)]) == gen, bar);
;             __builtin_amdgcn_fence(__ATOMIC_ACQUIRE, "agent");
;             asm volatile("s_waitcnt vmcnt(0)" ::: "memory");
;         }
.LBB0_689:
	s_or_b64 exec, exec, s[10:11]
	v_cvt_f32_u32_e32 v6, v4
	s_waitcnt vmcnt(0)
	v_readfirstlane_b32 s8, v5
	v_sub_u32_e32 v5, 0, v4
	v_rcp_iflag_f32_e32 v6, v6
	v_add_u32_e32 v7, s8, v3
	v_mul_f32_e32 v6, 0x4f7ffffe, v6
	v_cvt_u32_f32_e32 v6, v6
	v_mul_lo_u32 v3, v5, v6
	v_mul_hi_u32 v3, v6, v3
	v_add_u32_e32 v3, v6, v3
	v_mul_hi_u32 v3, v7, v3
	v_mul_lo_u32 v5, v3, v4
	v_sub_u32_e32 v5, v7, v5
	v_add_u32_e32 v6, 1, v3
	v_cmp_ge_u32_e32 vcc, v5, v4
	s_nop 1
	v_cndmask_b32_e32 v3, v3, v6, vcc
	v_sub_u32_e32 v6, v5, v4
	v_cndmask_b32_e32 v5, v5, v6, vcc
	v_add_u32_e32 v6, 1, v3
	v_cmp_ge_u32_e32 vcc, v5, v4
	v_add_u32_e32 v5, 1, v7
	s_nop 0
	v_cndmask_b32_e32 v3, v3, v6, vcc
	v_mul_lo_u32 v6, v4, v3
	v_add_u32_e32 v4, v6, v4
	v_cmp_ne_u32_e32 vcc, v5, v4
	s_and_saveexec_b64 s[8:9], vcc
	s_xor_b64 s[8:9], exec, s[8:9]
	s_cbranch_execz .LBB0_703
	s_waitcnt lgkmcnt(0)
	s_add_u32 s20, s34, 0x7500
	s_addc_u32 s21, s35, 0
	v_mov_b32_e32 v2, 0
	global_load_dword v2, v2, s[20:21] sc1
	s_waitcnt vmcnt(0)
	v_cmp_eq_u32_e32 vcc, v2, v3
	s_and_saveexec_b64 s[10:11], vcc
	s_cbranch_execz .LBB0_702
	s_add_u32 s14, s34, 0x4200
	s_addc_u32 s15, s35, 0
	s_mov_b32 s16, 1
	s_mov_b64 s[22:23], 0
	s_branch .LBB0_693

; __device__ __forceinline__ unsigned xb_ld(unsigned* p)              { return __hip_atomic_load(p, __ATOMIC_RELAXED, __HIP_MEMORY_SCOPE_AGENT); }
; __device__ __forceinline__ unsigned xb_add(unsigned* p, unsigned v) { return __hip_atomic_fetch_add(p, v, __ATOMIC_RELAXED, __HIP_MEMORY_SCOPE_AGENT); }
; #define XB_SPIN(cond, bar) do { unsigned _sp = 0; while (cond) { __builtin_amdgcn_s_sleep(1); \
;     if ((++_sp & 255u) == 0u) { if (xb_ld(&(bar)[XB_TMO])) break; if (_sp > XB_SPIN_CAP) { atomicAdd(&(bar)[XB_TMO], 1u); break; } } } } while (0)
; __device__ __forceinline__ void xcd_barrier(const XcdBarrier& b) {
;     ...
;         const unsigned old = xb_add(&bar[XB_XSUB(b.x)], 1u);
;         const unsigned gen = old / nloc;
;         if (old + 1u == (gen + 1u) * nloc) {
;             __builtin_amdgcn_fence(__ATOMIC_RELEASE, "agent");
;             asm volatile("s_waitcnt vmcnt(0)" ::: "memory");
;             const unsigned og = xb_add(&bar[XB_TOP], 1u);
;             const unsigned tg = og / nx;
;             if (og + 1u == (tg + 1u) * nx) xb_add(&bar[XB_TOPGEN], 1u);
;             else XB_SPIN(xb_ld(&bar[XB_TOPGEN]) == tg, bar);
;             __builtin_amdgcn_fence(__ATOMIC_ACQUIRE, "agent");
;             xb_add(&bar[XB_XGEN(b.x)], 1u);
;             asm volatile("s_waitcnt vmcnt(0)" ::: "memory");
;         } else {
;             XB_SPIN(xb_ld(&bar[XB_XGEN(b.x)]) == gen, bar);
;             __builtin_amdgcn_fence(__ATOMIC_ACQUIRE, "agent");
;             asm volatile("s_waitcnt vmcnt(0)" ::: "memory");
;         }
.LBB0_774:
	s_or_b64 exec, exec, s[14:15]
	v_cvt_f32_u32_e32 v5, v3
	s_waitcnt vmcnt(0)
	v_readfirstlane_b32 s3, v4
	v_sub_u32_e32 v4, 0, v3
	v_rcp_iflag_f32_e32 v5, v5
	v_add_u32_e32 v6, s3, v1
	v_mul_f32_e32 v5, 0x4f7ffffe, v5
	v_cvt_u32_f32_e32 v5, v5
	v_mul_lo_u32 v1, v4, v5
	v_mul_hi_u32 v1, v5, v1
	v_add_u32_e32 v1, v5, v1
	v_mul_hi_u32 v1, v6, v1
	v_mul_lo_u32 v4, v1, v3
	v_sub_u32_e32 v4, v6, v4
	v_add_u32_e32 v5, 1, v1
	v_cmp_ge_u32_e32 vcc, v4, v3
	s_nop 1
	v_cndmask_b32_e32 v1, v1, v5, vcc
	v_sub_u32_e32 v5, v4, v3
	v_cndmask_b32_e32 v4, v4, v5, vcc
	v_add_u32_e32 v5, 1, v1
	v_cmp_ge_u32_e32 vcc, v4, v3
	v_add_u32_e32 v4, 1, v6
	s_nop 0
	v_cndmask_b32_e32 v1, v1, v5, vcc
	v_mul_lo_u32 v5, v3, v1
	v_add_u32_e32 v3, v5, v3
	v_cmp_ne_u32_e32 vcc, v4, v3
	s_and_saveexec_b64 s[8:9], vcc
	s_xor_b64 s[8:9], exec, s[8:9]
	s_cbranch_execz .LBB0_788
	s_waitcnt lgkmcnt(0)
	s_add_u32 s22, s34, 0x7500
	s_addc_u32 s23, s35, 0
	v_mov_b32_e32 v2, 0
	global_load_dword v2, v2, s[22:23] sc1
	s_waitcnt vmcnt(0)
	v_cmp_eq_u32_e32 vcc, v2, v1
	s_and_saveexec_b64 s[14:15], vcc
	s_cbranch_execz .LBB0_787
	s_add_u32 s20, s34, 0x4200
	s_addc_u32 s21, s35, 0
	s_mov_b32 s3, 1
	s_mov_b64 s[26:27], 0
	s_branch .LBB0_778

; __device__ __forceinline__ unsigned xb_ld(unsigned* p)              { return __hip_atomic_load(p, __ATOMIC_RELAXED, __HIP_MEMORY_SCOPE_AGENT); }
; __device__ __forceinline__ unsigned xb_add(unsigned* p, unsigned v) { return __hip_atomic_fetch_add(p, v, __ATOMIC_RELAXED, __HIP_MEMORY_SCOPE_AGENT); }
; #define XB_SPIN(cond, bar) do { unsigned _sp = 0; while (cond) { __builtin_amdgcn_s_sleep(1); \
;     if ((++_sp & 255u) == 0u) { if (xb_ld(&(bar)[XB_TMO])) break; if (_sp > XB_SPIN_CAP) { atomicAdd(&(bar)[XB_TMO], 1u); break; } } } } while (0)
; __device__ __forceinline__ void xcd_barrier(const XcdBarrier& b) {
;     ...
;         const unsigned old = xb_add(&bar[XB_XSUB(b.x)], 1u);
;         const unsigned gen = old / nloc;
;         if (old + 1u == (gen + 1u) * nloc) {
;             __builtin_amdgcn_fence(__ATOMIC_RELEASE, "agent");
;             asm volatile("s_waitcnt vmcnt(0)" ::: "memory");
;             const unsigned og = xb_add(&bar[XB_TOP], 1u);
;             const unsigned tg = og / nx;
;             if (og + 1u == (tg + 1u) * nx) xb_add(&bar[XB_TOPGEN], 1u);
;             else XB_SPIN(xb_ld(&bar[XB_TOPGEN]) == tg, bar);
;             __builtin_amdgcn_fence(__ATOMIC_ACQUIRE, "agent");
;             xb_add(&bar[XB_XGEN(b.x)], 1u);
;             asm volatile("s_waitcnt vmcnt(0)" ::: "memory");
;         } else {
;             XB_SPIN(xb_ld(&bar[XB_XGEN(b.x)]) == gen, bar);
;             __builtin_amdgcn_fence(__ATOMIC_ACQUIRE, "agent");
;             asm volatile("s_waitcnt vmcnt(0)" ::: "memory");
;         }
.LBB0_901:
	s_or_b64 exec, exec, s[14:15]
	v_cvt_f32_u32_e32 v5, v3
	s_waitcnt vmcnt(0)
	v_readfirstlane_b32 s3, v4
	v_sub_u32_e32 v4, 0, v3
	v_rcp_iflag_f32_e32 v5, v5
	v_add_u32_e32 v6, s3, v1
	v_mul_f32_e32 v5, 0x4f7ffffe, v5
	v_cvt_u32_f32_e32 v5, v5
	v_mul_lo_u32 v1, v4, v5
	v_mul_hi_u32 v1, v5, v1
	v_add_u32_e32 v1, v5, v1
	v_mul_hi_u32 v1, v6, v1
	v_mul_lo_u32 v4, v1, v3
	v_sub_u32_e32 v4, v6, v4
	v_add_u32_e32 v5, 1, v1
	v_cmp_ge_u32_e32 vcc, v4, v3
	s_nop 1
	v_cndmask_b32_e32 v1, v1, v5, vcc
	v_sub_u32_e32 v5, v4, v3
	v_cndmask_b32_e32 v4, v4, v5, vcc
	v_add_u32_e32 v5, 1, v1
	v_cmp_ge_u32_e32 vcc, v4, v3
	v_add_u32_e32 v4, 1, v6
	s_nop 0
	v_cndmask_b32_e32 v1, v1, v5, vcc
	v_mul_lo_u32 v5, v3, v1
	v_add_u32_e32 v3, v5, v3
	v_cmp_ne_u32_e32 vcc, v4, v3
	s_and_saveexec_b64 s[8:9], vcc
	s_xor_b64 s[8:9], exec, s[8:9]
	s_cbranch_execz .LBB0_915
	s_waitcnt lgkmcnt(0)
	s_add_u32 s26, s34, 0x7500
	s_addc_u32 s27, s35, 0
	v_mov_b32_e32 v2, 0
	global_load_dword v2, v2, s[26:27] sc1
	s_waitcnt vmcnt(0)
	v_cmp_eq_u32_e32 vcc, v2, v1
	s_and_saveexec_b64 s[14:15], vcc
	s_cbranch_execz .LBB0_914
	s_add_u32 s22, s34, 0x4200
	s_addc_u32 s23, s35, 0
	s_mov_b32 s3, 1
	s_mov_b64 s[28:29], 0
	s_branch .LBB0_905

; #define LAS __attribute__((address_space(3)))
; __device__ __forceinline__ unsigned cvtpk(float lo, float hi) { f32x2 v = {lo, hi}; bf16x2_t b = __builtin_convertvector(v, bf16x2_t); return __builtin_bit_cast(unsigned, b); }
; #define ATT_SB() __builtin_amdgcn_sched_barrier(0)
; #define ATT_VLOAD(sl, h_) do { _Pragma("unroll") for (int g_ = 0; g_ < NVF; ++g_) { \
;         if constexpr (KS) vf[g_] = *(const LAS bf16x8*)(vpk + (sl) * VSLOT + g_ * 2048); \
;         else vf[g_] = *(const LAS bf16x8*)(vp[g_ & 1] + (sl) * VSLOT + ((h_) * 4 + (g_ >> 1)) * 2048); } } while (0)
; template <int DQK, int DV, bool LEAD> ...
;     ...
;     ATT_VLOAD(s_prev, 0); ATT_PVP(0);
;     if constexpr (DV == 128) { ATT_SB(); ATT_VLOAD(s_prev, 1); ATT_PVP(1); }
; #pragma unroll
;     for (int qb = 0; qb < NQB; ++qb) lsum[qb] = lanes4_sum(lsum[qb]);
;     if constexpr (KS) {
;         wait_bar<0>();
;         LAS unsigned char* xch = shm + (wid & 3) * 17408;
;         if constexpr (!LEAD) {
; #pragma unroll
;             for (int db = 0; db < 4; ++db)
; #pragma unroll
;                 for (int qb = 0; qb < 4; ++qb) *(LAS f32x4*)(xch + ((db * 4 + qb) * 64 + lane) * 16) = o[db][qb];
; #pragma unroll
;             for (int qb = 0; qb < 4; ++qb) *(LAS float*)(xch + 16384 + (qb * 64 + lane) * 4) = lsum[qb];
;         }
;         asm volatile("s_waitcnt lgkmcnt(0)\n\ts_barrier" ::: "memory");
;         if constexpr (LEAD) {
;             float inv[4];
; #pragma unroll
;             for (int qb = 0; qb < 4; ++qb) inv[qb] = 1.0f / (lsum[qb] + *(const LAS float*)(xch + 16384 + (qb * 64 + lane) * 4));
;             LAS unsigned char* stg = shm + ATT_LDS + (wid & 3) * 8192;
; #pragma unroll
;             for (int dbl = 0; dbl < 4; ++dbl)
; #pragma unroll
;                 for (int qb = 0; qb < 4; ++qb) { const f32x4 ov = o[dbl][qb] + *(const LAS f32x4*)(xch + ((dbl * 4 + qb) * 64 + lane) * 16); const int row = qb * 16 + q16;
;                     u32x2 w; w.x = cvtpk(ov[0] * inv[qb], ov[1] * inv[qb]); w.y = cvtpk(ov[2] * inv[qb], ov[3] * inv[qb]);
;                     *(LAS u32x2*)(stg + row * 128 + (((4 * dbl + g4) ^ ((row & 7) << 1)) << 3)) = w; }
.LBB0_953:
	v_add_u32_e32 v14, s16, v177
	ds_read_b128 v[2:5], v14 offset:36864
	ds_read_b128 v[6:9], v14 offset:38912
	ds_read_b128 v[10:13], v14 offset:40960
	ds_read_b128 v[130:133], v14 offset:43008
	s_lshl_b32 s4, s26, 1
	s_waitcnt lgkmcnt(3)
	v_mfma_f32_16x16x32_bf16 v[118:121], v[2:5], v[102:105], v[118:121]
	s_add_u32 s4, s30, s4
	s_addc_u32 s5, s31, 0
	s_add_u32 s4, s4, s43
	v_mfma_f32_16x16x32_bf16 v[110:113], v[2:5], v[114:117], v[110:113]
	s_mul_i32 s16, s7, 0x4400
	s_addc_u32 s5, s5, 0
	s_waitcnt vmcnt(0) lgkmcnt(0)
	s_barrier
	v_mfma_f32_16x16x32_bf16 v[106:109], v[2:5], v[122:125], v[106:109]
	s_add_i32 s16, s16, 0
	s_waitcnt lgkmcnt(0)
	s_barrier
	s_lshl_b32 s7, s7, 13
	v_mfma_f32_16x16x32_bf16 v[98:101], v[2:5], v[126:129], v[98:101]
	s_add_i32 s7, s7, 0
	s_add_i32 s7, s7, 0x15000
	v_lshlrev_b32_e32 v194, 4, v170
	s_waitcnt lgkmcnt(0)
	v_mfma_f32_16x16x32_bf16 v[2:5], v[130:133], v[126:129], v[50:53]
	s_nop 2
	v_mov_b32_e32 v50, v169
	s_nop 1
	v_permlane16_swap_b32_e32 v169, v50
	v_add_f32_e32 v50, v169, v50
	v_mov_b32_e32 v51, v50
	s_nop 1
	v_permlane32_swap_b32_e32 v50, v51
	v_add_f32_e32 v52, v50, v51
	v_mov_b32_e32 v50, v168
	s_nop 1
	v_permlane16_swap_b32_e32 v168, v50
	v_add_f32_e32 v50, v168, v50
	v_mov_b32_e32 v51, v50
	s_nop 1
	v_permlane32_swap_b32_e32 v50, v51
	v_add_f32_e32 v53, v50, v51
	v_mov_b32_e32 v50, v167
	s_nop 1
	v_permlane16_swap_b32_e32 v167, v50
	v_add_f32_e32 v50, v167, v50
	v_mov_b32_e32 v51, v50
	s_nop 1
	v_permlane32_swap_b32_e32 v50, v51
	v_mfma_f32_16x16x32_bf16 v[46:49], v[6:9], v[102:105], v[94:97]
	v_mfma_f32_16x16x32_bf16 v[42:45], v[6:9], v[114:117], v[90:93]
	v_mfma_f32_16x16x32_bf16 v[38:41], v[6:9], v[122:125], v[86:89]
	v_mfma_f32_16x16x32_bf16 v[34:37], v[6:9], v[126:129], v[82:85]
	v_mfma_f32_16x16x32_bf16 v[6:9], v[130:133], v[122:125], v[54:57]
	s_nop 2
	v_add_f32_e32 v56, v50, v51
	v_mov_b32_e32 v50, v166
	s_nop 1
	v_permlane16_swap_b32_e32 v166, v50
	v_add_f32_e32 v50, v166, v50
	v_mov_b32_e32 v51, v50
	s_nop 1
	v_permlane32_swap_b32_e32 v50, v51
	v_lshl_add_u32 v54, v174, 2, s16
	v_add_f32_e32 v57, v50, v51
	ds_read2st64_b32 v[50:51], v54 offset0:64 offset1:65
	v_mfma_f32_16x16x32_bf16 v[30:33], v[10:13], v[102:105], v[78:81]
	s_waitcnt lgkmcnt(0)
	v_add_f32_e32 v50, v52, v50
	v_div_scale_f32 v52, s[26:27], v50, v50, 1.0
	v_rcp_f32_e32 v55, v52
	v_mfma_f32_16x16x32_bf16 v[26:29], v[10:13], v[114:117], v[74:77]
	v_mfma_f32_16x16x32_bf16 v[22:25], v[10:13], v[122:125], v[70:73]
	v_mfma_f32_16x16x32_bf16 v[18:21], v[10:13], v[126:129], v[66:69]
	v_mfma_f32_16x16x32_bf16 v[10:13], v[130:133], v[114:117], v[58:61]
	s_nop 2
	v_fma_f32 v58, -v52, v55, 1.0
	v_fmac_f32_e32 v55, v58, v55
	v_div_scale_f32 v58, vcc, 1.0, v50, 1.0
	v_mul_f32_e32 v59, v58, v55
	v_fma_f32 v60, -v52, v59, v58
	v_fmac_f32_e32 v59, v60, v55
	v_fma_f32 v52, -v52, v59, v58
	v_div_fmas_f32 v52, v52, v55, v59
	v_div_fixup_f32 v52, v52, v50, 1.0
	v_add_f32_e32 v50, v53, v51
	v_div_scale_f32 v51, s[26:27], v50, v50, 1.0
	v_rcp_f32_e32 v53, v51
	v_mfma_f32_16x16x32_bf16 v[14:17], v[130:133], v[102:105], v[62:65]
	v_fma_f32 v55, -v51, v53, 1.0
	v_fmac_f32_e32 v53, v55, v53
	v_div_scale_f32 v55, vcc, 1.0, v50, 1.0
	v_mul_f32_e32 v58, v55, v53
	v_fma_f32 v59, -v51, v58, v55
	v_fmac_f32_e32 v58, v59, v53
	v_fma_f32 v51, -v51, v58, v55
	ds_read2st64_b32 v[54:55], v54 offset0:66 offset1:67
	v_div_fmas_f32 v51, v51, v53, v58
	v_div_fixup_f32 v50, v51, v50, 1.0
	s_waitcnt lgkmcnt(0)
	v_add_f32_e32 v51, v56, v54
	v_div_scale_f32 v53, s[26:27], v51, v51, 1.0
	v_rcp_f32_e32 v54, v53
	s_nop 0
	v_fma_f32 v56, -v53, v54, 1.0
	v_fmac_f32_e32 v54, v56, v54
	v_div_scale_f32 v56, vcc, 1.0, v51, 1.0
	v_mul_f32_e32 v58, v56, v54
	v_fma_f32 v59, -v53, v58, v56
	v_fmac_f32_e32 v58, v59, v54
	v_fma_f32 v53, -v53, v58, v56
	v_div_fmas_f32 v53, v53, v54, v58
	v_div_fixup_f32 v56, v53, v51, 1.0
	v_add_f32_e32 v51, v57, v55
	v_div_scale_f32 v53, s[26:27], v51, v51, 1.0
	v_rcp_f32_e32 v54, v53
	s_nop 0
	v_fma_f32 v55, -v53, v54, 1.0
	v_fmac_f32_e32 v54, v55, v54
	v_div_scale_f32 v55, vcc, 1.0, v51, 1.0
	v_mul_f32_e32 v57, v55, v54
	v_fma_f32 v58, -v53, v57, v55
	v_fmac_f32_e32 v57, v58, v54
	v_fma_f32 v53, -v53, v57, v55
	v_div_fmas_f32 v53, v53, v54, v57
	v_div_fixup_f32 v54, v53, v51, 1.0
	v_lshl_add_u32 v51, v174, 4, s16
	ds_read_b128 v[134:137], v51
	ds_read_b128 v[138:141], v51 offset:1024
	ds_read_b128 v[142:145], v51 offset:2048
	ds_read_b128 v[146:149], v51 offset:3072
	ds_read_b128 v[150:153], v51 offset:4096
	ds_read_b128 v[154:157], v51 offset:5120
	ds_read_b128 v[158:161], v51 offset:6144
	ds_read_b128 v[180:183], v51 offset:7168
	v_add_u32_e32 v53, s7, v173
	v_bitop3_b32 v57, v171, v172, 14 bitop3:0x78
	v_lshl_add_u32 v57, v57, 3, v53
	v_and_b32_e32 v55, 14, v172
	s_waitcnt lgkmcnt(4)
	v_pk_add_f32 v[58:59], v[118:119], v[134:135]
	v_pk_add_f32 v[60:61], v[120:121], v[136:137]
	v_pk_mul_f32 v[58:59], v[52:53], v[58:59] op_sel_hi:[0,1]
	v_cvt_pk_bf16_f32 v62, v58, v59
	v_pk_mul_f32 v[58:59], v[52:53], v[60:61] op_sel_hi:[0,1]
	v_cvt_pk_bf16_f32 v63, v58, v59
	v_pk_add_f32 v[60:61], v[112:113], v[140:141]
	v_pk_add_f32 v[58:59], v[110:111], v[138:139]
	v_pk_mul_f32 v[60:61], v[50:51], v[60:61] op_sel_hi:[0,1]
	v_pk_mul_f32 v[58:59], v[50:51], v[58:59] op_sel_hi:[0,1]
	v_cvt_pk_bf16_f32 v58, v58, v59
	v_cvt_pk_bf16_f32 v59, v60, v61
	ds_write2st64_b64 v57, v[62:63], v[58:59] offset1:4
	v_pk_add_f32 v[58:59], v[106:107], v[142:143]
	v_pk_add_f32 v[60:61], v[108:109], v[144:145]
	v_pk_mul_f32 v[58:59], v[56:57], v[58:59] op_sel_hi:[0,1]
	v_cvt_pk_bf16_f32 v62, v58, v59
	v_pk_mul_f32 v[58:59], v[56:57], v[60:61] op_sel_hi:[0,1]
	v_cvt_pk_bf16_f32 v63, v58, v59
	v_pk_add_f32 v[60:61], v[100:101], v[148:149]
	v_pk_add_f32 v[58:59], v[98:99], v[146:147]
	v_pk_mul_f32 v[60:61], v[54:55], v[60:61] op_sel_hi:[0,1]
	v_pk_mul_f32 v[58:59], v[54:55], v[58:59] op_sel_hi:[0,1]
	v_cvt_pk_bf16_f32 v58, v58, v59
	v_cvt_pk_bf16_f32 v59, v60, v61
	ds_write2st64_b64 v57, v[62:63], v[58:59] offset0:8 offset1:12
	ds_read_b128 v[134:137], v51 offset:8192
	ds_read_b128 v[138:141], v51 offset:9216
	ds_read_b128 v[142:145], v51 offset:10240
	ds_read_b128 v[146:149], v51 offset:11264
	v_bitop3_b32 v57, v176, v172, 14 bitop3:0x78
	v_lshl_add_u32 v57, v57, 3, v53
	s_waitcnt lgkmcnt(6)
; #define LAS __attribute__((address_space(3)))
; __device__ __forceinline__ unsigned cvtpk(float lo, float hi) { f32x2 v = {lo, hi}; bf16x2_t b = __builtin_convertvector(v, bf16x2_t); return __builtin_bit_cast(unsigned, b); }
; template <int DQK, int DV, bool LEAD> ...
;     ...
;             for (int qb = 0; qb < 4; ++qb) inv[qb] = 1.0f / (lsum[qb] + *(const LAS float*)(xch + 16384 + (qb * 64 + lane) * 4));
;             LAS unsigned char* stg = shm + ATT_LDS + (wid & 3) * 8192;
; #pragma unroll
;             for (int dbl = 0; dbl < 4; ++dbl)
; #pragma unroll
;                 for (int qb = 0; qb < 4; ++qb) { const f32x4 ov = o[dbl][qb] + *(const LAS f32x4*)(xch + ((dbl * 4 + qb) * 64 + lane) * 16); const int row = qb * 16 + q16;
;                     u32x2 w; w.x = cvtpk(ov[0] * inv[qb], ov[1] * inv[qb]); w.y = cvtpk(ov[2] * inv[qb], ov[3] * inv[qb]);
;                     *(LAS u32x2*)(stg + row * 128 + (((4 * dbl + g4) ^ ((row & 7) << 1)) << 3)) = w; }
;             asm volatile("s_waitcnt lgkmcnt(0)" ::: "memory");
; #pragma unroll
;             for (int rr = 0; rr < 8; ++rr) { const int row = rr * 8 + (lane >> 3), ch = lane & 7;
;                 const u32x4 v = *(const LAS u32x4*)(stg + row * 128 + ((ch ^ (row & 7)) << 4));
;                 *(u32x4*)(O + (size_t)(qrow0 + qoff + row) * opitch + ch * 8) = v; }
;             asm volatile("s_waitcnt lgkmcnt(0)" ::: "memory");
	v_pk_add_f32 v[46:47], v[46:47], v[150:151]
	v_pk_add_f32 v[48:49], v[48:49], v[152:153]
	v_pk_mul_f32 v[46:47], v[52:53], v[46:47] op_sel_hi:[0,1]
	v_cvt_pk_bf16_f32 v58, v46, v47
	v_pk_mul_f32 v[46:47], v[52:53], v[48:49] op_sel_hi:[0,1]
	v_cvt_pk_bf16_f32 v59, v46, v47
	v_pk_add_f32 v[44:45], v[44:45], v[156:157]
	v_pk_add_f32 v[42:43], v[42:43], v[154:155]
	v_pk_mul_f32 v[44:45], v[50:51], v[44:45] op_sel_hi:[0,1]
	v_pk_mul_f32 v[42:43], v[50:51], v[42:43] op_sel_hi:[0,1]
	v_cvt_pk_bf16_f32 v42, v42, v43
	v_cvt_pk_bf16_f32 v43, v44, v45
	ds_write2st64_b64 v57, v[58:59], v[42:43] offset1:4
	v_pk_add_f32 v[38:39], v[38:39], v[158:159]
	v_pk_add_f32 v[40:41], v[40:41], v[160:161]
	v_pk_mul_f32 v[38:39], v[56:57], v[38:39] op_sel_hi:[0,1]
	v_cvt_pk_bf16_f32 v42, v38, v39
	v_pk_mul_f32 v[38:39], v[56:57], v[40:41] op_sel_hi:[0,1]
	v_cvt_pk_bf16_f32 v43, v38, v39
	v_pk_add_f32 v[36:37], v[36:37], v[182:183]
	v_pk_add_f32 v[34:35], v[34:35], v[180:181]
	v_pk_mul_f32 v[36:37], v[54:55], v[36:37] op_sel_hi:[0,1]
	v_pk_mul_f32 v[34:35], v[54:55], v[34:35] op_sel_hi:[0,1]
	v_cvt_pk_bf16_f32 v34, v34, v35
	v_cvt_pk_bf16_f32 v35, v36, v37
	ds_write2st64_b64 v57, v[42:43], v[34:35] offset0:8 offset1:12
	v_bitop3_b32 v34, v171, v55, 8 bitop3:0x36
	v_lshl_add_u32 v38, v34, 3, v53
	ds_read_b128 v[150:153], v51 offset:12288
	ds_read_b128 v[154:157], v51 offset:13312
	ds_read_b128 v[158:161], v51 offset:14336
	ds_read_b128 v[180:183], v51 offset:15360
	s_waitcnt lgkmcnt(6)
	v_pk_add_f32 v[30:31], v[30:31], v[134:135]
	v_pk_add_f32 v[32:33], v[32:33], v[136:137]
	v_pk_mul_f32 v[30:31], v[52:53], v[30:31] op_sel_hi:[0,1]
	v_cvt_pk_bf16_f32 v34, v30, v31
	v_pk_mul_f32 v[30:31], v[52:53], v[32:33] op_sel_hi:[0,1]
	v_cvt_pk_bf16_f32 v35, v30, v31
	v_pk_add_f32 v[28:29], v[28:29], v[140:141]
	v_pk_add_f32 v[26:27], v[26:27], v[138:139]
	v_pk_mul_f32 v[28:29], v[50:51], v[28:29] op_sel_hi:[0,1]
	v_pk_mul_f32 v[26:27], v[50:51], v[26:27] op_sel_hi:[0,1]
	v_cvt_pk_bf16_f32 v26, v26, v27
	v_cvt_pk_bf16_f32 v27, v28, v29
	ds_write2st64_b64 v38, v[34:35], v[26:27] offset1:4
	v_pk_add_f32 v[22:23], v[22:23], v[142:143]
	v_pk_add_f32 v[24:25], v[24:25], v[144:145]
	v_pk_mul_f32 v[22:23], v[56:57], v[22:23] op_sel_hi:[0,1]
	v_cvt_pk_bf16_f32 v26, v22, v23
	v_pk_mul_f32 v[22:23], v[56:57], v[24:25] op_sel_hi:[0,1]
	v_cvt_pk_bf16_f32 v27, v22, v23
	v_pk_add_f32 v[20:21], v[20:21], v[148:149]
	v_pk_add_f32 v[18:19], v[18:19], v[146:147]
	v_pk_mul_f32 v[20:21], v[54:55], v[20:21] op_sel_hi:[0,1]
	v_pk_mul_f32 v[18:19], v[54:55], v[18:19] op_sel_hi:[0,1]
	v_cvt_pk_bf16_f32 v18, v18, v19
	v_cvt_pk_bf16_f32 v19, v20, v21
	ds_write2st64_b64 v38, v[26:27], v[18:19] offset0:8 offset1:12
	v_bitop3_b32 v18, v171, v55, 12 bitop3:0x36
	v_lshl_add_u32 v22, v18, 3, v53
	s_waitcnt lgkmcnt(2)
	v_pk_add_f32 v[14:15], v[14:15], v[150:151]
	v_pk_add_f32 v[16:17], v[16:17], v[152:153]
	v_pk_mul_f32 v[14:15], v[52:53], v[14:15] op_sel_hi:[0,1]
	v_cvt_pk_bf16_f32 v18, v14, v15
	v_pk_mul_f32 v[14:15], v[52:53], v[16:17] op_sel_hi:[0,1]
	v_cvt_pk_bf16_f32 v19, v14, v15
	v_pk_add_f32 v[12:13], v[12:13], v[156:157]
	v_pk_add_f32 v[10:11], v[10:11], v[154:155]
	v_pk_mul_f32 v[12:13], v[50:51], v[12:13] op_sel_hi:[0,1]
	v_pk_mul_f32 v[10:11], v[50:51], v[10:11] op_sel_hi:[0,1]
	v_cvt_pk_bf16_f32 v10, v10, v11
	v_cvt_pk_bf16_f32 v11, v12, v13
	ds_write2st64_b64 v22, v[18:19], v[10:11] offset1:4
	v_pk_add_f32 v[6:7], v[6:7], v[158:159]
	v_pk_add_f32 v[8:9], v[8:9], v[160:161]
	v_pk_mul_f32 v[6:7], v[56:57], v[6:7] op_sel_hi:[0,1]
	v_cvt_pk_bf16_f32 v10, v6, v7
	v_pk_mul_f32 v[6:7], v[56:57], v[8:9] op_sel_hi:[0,1]
	v_cvt_pk_bf16_f32 v11, v6, v7
	v_pk_add_f32 v[4:5], v[4:5], v[182:183]
	v_pk_add_f32 v[2:3], v[2:3], v[180:181]
	v_pk_mul_f32 v[4:5], v[54:55], v[4:5] op_sel_hi:[0,1]
	v_pk_mul_f32 v[2:3], v[54:55], v[2:3] op_sel_hi:[0,1]
	v_cvt_pk_bf16_f32 v2, v2, v3
	v_cvt_pk_bf16_f32 v3, v4, v5
	ds_write2st64_b64 v22, v[10:11], v[2:3] offset0:8 offset1:12
	v_xor_b32_e32 v2, v1, v170
	v_lshl_add_u32 v10, v2, 4, s7
	s_waitcnt lgkmcnt(0)
	v_lshl_add_u32 v2, v1, 7, v10
	ds_read_b128 v[134:137], v2
	v_or_b32_e32 v8, 8, v1
	v_lshl_add_u32 v2, v8, 7, v10
	ds_read_b128 v[138:141], v2
	v_or_b32_e32 v8, 16, v1
	v_lshl_add_u32 v2, v8, 7, v10
	ds_read_b128 v[142:145], v2
	v_or_b32_e32 v8, 24, v1
	v_lshl_add_u32 v2, v8, 7, v10
	ds_read_b128 v[146:149], v2
	v_or_b32_e32 v8, 32, v1
	v_lshl_add_u32 v2, v8, 7, v10
	ds_read_b128 v[150:153], v2
	v_or_b32_e32 v8, 40, v1
	v_lshl_add_u32 v2, v8, 7, v10
	ds_read_b128 v[154:157], v2
	v_or_b32_e32 v8, 48, v1
	v_lshl_add_u32 v2, v8, 7, v10
	ds_read_b128 v[158:161], v2
	v_or_b32_e32 v8, 56, v1
	v_lshl_add_u32 v2, v8, 7, v10
	ds_read_b128 v[180:183], v2
	v_lshl_add_u64 v[6:7], s[4:5], 0, v[194:195]
	v_or_b32_e32 v8, s6, v1
	v_ashrrev_i32_e32 v9, 31, v8
	v_lshlrev_b64 v[8:9], 11, v[8:9]
	v_lshl_add_u64 v[8:9], v[6:7], 0, v[8:9]
	s_waitcnt lgkmcnt(7)
	global_store_dwordx4 v[8:9], v[134:137], off
	v_or_b32_e32 v8, 8, v1
	v_or_b32_e32 v8, s6, v8
	v_ashrrev_i32_e32 v9, 31, v8
	v_lshlrev_b64 v[8:9], 11, v[8:9]
	v_lshl_add_u64 v[8:9], v[6:7], 0, v[8:9]
	s_waitcnt lgkmcnt(6)
	global_store_dwordx4 v[8:9], v[138:141], off
	v_or_b32_e32 v8, 16, v1
	v_or_b32_e32 v8, s6, v8
	v_ashrrev_i32_e32 v9, 31, v8
	v_lshlrev_b64 v[8:9], 11, v[8:9]
	v_lshl_add_u64 v[8:9], v[6:7], 0, v[8:9]
	s_waitcnt lgkmcnt(5)
	global_store_dwordx4 v[8:9], v[142:145], off
	v_or_b32_e32 v8, 24, v1
	v_or_b32_e32 v8, s6, v8
	v_ashrrev_i32_e32 v9, 31, v8
	v_lshlrev_b64 v[8:9], 11, v[8:9]
	v_lshl_add_u64 v[8:9], v[6:7], 0, v[8:9]
	s_waitcnt lgkmcnt(4)
	global_store_dwordx4 v[8:9], v[146:149], off
	v_or_b32_e32 v8, 32, v1
	v_or_b32_e32 v8, s6, v8
	v_ashrrev_i32_e32 v9, 31, v8
	v_lshlrev_b64 v[8:9], 11, v[8:9]
	v_lshl_add_u64 v[8:9], v[6:7], 0, v[8:9]
	s_waitcnt lgkmcnt(3)
	global_store_dwordx4 v[8:9], v[150:153], off
	v_or_b32_e32 v8, 40, v1
	v_or_b32_e32 v8, s6, v8
	v_ashrrev_i32_e32 v9, 31, v8
	v_lshlrev_b64 v[8:9], 11, v[8:9]
	v_lshl_add_u64 v[8:9], v[6:7], 0, v[8:9]
	s_waitcnt lgkmcnt(2)
	global_store_dwordx4 v[8:9], v[154:157], off
	v_or_b32_e32 v8, 48, v1
	v_or_b32_e32 v8, s6, v8
	v_ashrrev_i32_e32 v9, 31, v8
	v_lshlrev_b64 v[8:9], 11, v[8:9]
	v_lshl_add_u64 v[8:9], v[6:7], 0, v[8:9]
	s_waitcnt lgkmcnt(1)
	global_store_dwordx4 v[8:9], v[158:161], off
	v_or_b32_e32 v8, 56, v1
	v_or_b32_e32 v8, s6, v8
	v_ashrrev_i32_e32 v9, 31, v8
	v_lshlrev_b64 v[8:9], 11, v[8:9]
	v_lshl_add_u64 v[8:9], v[6:7], 0, v[8:9]
	s_waitcnt lgkmcnt(0)
	global_store_dwordx4 v[8:9], v[180:183], off
	s_waitcnt lgkmcnt(0)
	s_waitcnt lgkmcnt(0)
	s_barrier

; __device__ __forceinline__ unsigned xb_ld(unsigned* p)              { return __hip_atomic_load(p, __ATOMIC_RELAXED, __HIP_MEMORY_SCOPE_AGENT); }
; __device__ __forceinline__ unsigned xb_add(unsigned* p, unsigned v) { return __hip_atomic_fetch_add(p, v, __ATOMIC_RELAXED, __HIP_MEMORY_SCOPE_AGENT); }
; #define XB_SPIN(cond, bar) do { unsigned _sp = 0; while (cond) { __builtin_amdgcn_s_sleep(1); \
;     if ((++_sp & 255u) == 0u) { if (xb_ld(&(bar)[XB_TMO])) break; if (_sp > XB_SPIN_CAP) { atomicAdd(&(bar)[XB_TMO], 1u); break; } } } } while (0)
; __device__ __forceinline__ void xcd_barrier(const XcdBarrier& b) {
;     ...
;         const unsigned old = xb_add(&bar[XB_XSUB(b.x)], 1u);
;         const unsigned gen = old / nloc;
;         if (old + 1u == (gen + 1u) * nloc) {
;             __builtin_amdgcn_fence(__ATOMIC_RELEASE, "agent");
;             asm volatile("s_waitcnt vmcnt(0)" ::: "memory");
;             const unsigned og = xb_add(&bar[XB_TOP], 1u);
;             const unsigned tg = og / nx;
;             if (og + 1u == (tg + 1u) * nx) xb_add(&bar[XB_TOPGEN], 1u);
;             else XB_SPIN(xb_ld(&bar[XB_TOPGEN]) == tg, bar);
;             __builtin_amdgcn_fence(__ATOMIC_ACQUIRE, "agent");
;             xb_add(&bar[XB_XGEN(b.x)], 1u);
;             asm volatile("s_waitcnt vmcnt(0)" ::: "memory");
;         } else {
;             XB_SPIN(xb_ld(&bar[XB_XGEN(b.x)]) == gen, bar);
;             __builtin_amdgcn_fence(__ATOMIC_ACQUIRE, "agent");
;             asm volatile("s_waitcnt vmcnt(0)" ::: "memory");
;         }
.LBB0_1018:
	s_or_b64 exec, exec, s[10:11]
	v_cvt_f32_u32_e32 v5, v3
	s_waitcnt vmcnt(0)
	v_readfirstlane_b32 s3, v4
	v_sub_u32_e32 v4, 0, v3
	v_rcp_iflag_f32_e32 v5, v5
	v_add_u32_e32 v6, s3, v1
	v_mul_f32_e32 v5, 0x4f7ffffe, v5
	v_cvt_u32_f32_e32 v5, v5
	v_mul_lo_u32 v1, v4, v5
	v_mul_hi_u32 v1, v5, v1
	v_add_u32_e32 v1, v5, v1
	v_mul_hi_u32 v1, v6, v1
	v_mul_lo_u32 v4, v1, v3
	v_sub_u32_e32 v4, v6, v4
	v_add_u32_e32 v5, 1, v1
	v_cmp_ge_u32_e32 vcc, v4, v3
	s_nop 1
	v_cndmask_b32_e32 v1, v1, v5, vcc
	v_sub_u32_e32 v5, v4, v3
	v_cndmask_b32_e32 v4, v4, v5, vcc
	v_add_u32_e32 v5, 1, v1
	v_cmp_ge_u32_e32 vcc, v4, v3
	v_add_u32_e32 v4, 1, v6
	s_nop 0
	v_cndmask_b32_e32 v1, v1, v5, vcc
	v_mul_lo_u32 v5, v3, v1
	v_add_u32_e32 v3, v5, v3
	v_cmp_ne_u32_e32 vcc, v4, v3
	s_and_saveexec_b64 s[8:9], vcc
	s_xor_b64 s[8:9], exec, s[8:9]
	s_cbranch_execz .LBB0_1032
	s_waitcnt lgkmcnt(0)
	s_add_u32 s14, s34, 0x7500
	s_addc_u32 s15, s35, 0
	v_mov_b32_e32 v2, 0
	global_load_dword v2, v2, s[14:15] sc1
	s_waitcnt vmcnt(0)
	v_cmp_eq_u32_e32 vcc, v2, v1
	s_and_saveexec_b64 s[10:11], vcc
	s_cbranch_execz .LBB0_1031
	s_add_u32 s12, s34, 0x4200
	s_addc_u32 s13, s35, 0
	s_mov_b32 s3, 1
	s_mov_b64 s[18:19], 0
	s_branch .LBB0_1022

; __device__ __forceinline__ unsigned xb_ld(unsigned* p)              { return __hip_atomic_load(p, __ATOMIC_RELAXED, __HIP_MEMORY_SCOPE_AGENT); }
; __device__ __forceinline__ unsigned xb_add(unsigned* p, unsigned v) { return __hip_atomic_fetch_add(p, v, __ATOMIC_RELAXED, __HIP_MEMORY_SCOPE_AGENT); }
; #define XB_SPIN(cond, bar) do { unsigned _sp = 0; while (cond) { __builtin_amdgcn_s_sleep(1); \
;     if ((++_sp & 255u) == 0u) { if (xb_ld(&(bar)[XB_TMO])) break; if (_sp > XB_SPIN_CAP) { atomicAdd(&(bar)[XB_TMO], 1u); break; } } } } while (0)
; __device__ __forceinline__ void xcd_barrier(const XcdBarrier& b) {
;     ...
;         const unsigned old = xb_add(&bar[XB_XSUB(b.x)], 1u);
;         const unsigned gen = old / nloc;
;         if (old + 1u == (gen + 1u) * nloc) {
;             __builtin_amdgcn_fence(__ATOMIC_RELEASE, "agent");
;             asm volatile("s_waitcnt vmcnt(0)" ::: "memory");
;             const unsigned og = xb_add(&bar[XB_TOP], 1u);
;             const unsigned tg = og / nx;
;             if (og + 1u == (tg + 1u) * nx) xb_add(&bar[XB_TOPGEN], 1u);
;             else XB_SPIN(xb_ld(&bar[XB_TOPGEN]) == tg, bar);
;             __builtin_amdgcn_fence(__ATOMIC_ACQUIRE, "agent");
;             xb_add(&bar[XB_XGEN(b.x)], 1u);
;             asm volatile("s_waitcnt vmcnt(0)" ::: "memory");
;         } else {
;             XB_SPIN(xb_ld(&bar[XB_XGEN(b.x)]) == gen, bar);
;             __builtin_amdgcn_fence(__ATOMIC_ACQUIRE, "agent");
;             asm volatile("s_waitcnt vmcnt(0)" ::: "memory");
;         }
.LBB0_1079:
	s_or_b64 exec, exec, s[10:11]
	v_cvt_f32_u32_e32 v6, v4
	s_waitcnt vmcnt(0)
	v_readfirstlane_b32 s2, v5
	v_sub_u32_e32 v5, 0, v4
	v_rcp_iflag_f32_e32 v6, v6
	v_add_u32_e32 v7, s2, v3
	v_mul_f32_e32 v6, 0x4f7ffffe, v6
	v_cvt_u32_f32_e32 v6, v6
	v_mul_lo_u32 v3, v5, v6
	v_mul_hi_u32 v3, v6, v3
	v_add_u32_e32 v3, v6, v3
	v_mul_hi_u32 v3, v7, v3
	v_mul_lo_u32 v5, v3, v4
	v_sub_u32_e32 v5, v7, v5
	v_add_u32_e32 v6, 1, v3
	v_cmp_ge_u32_e32 vcc, v5, v4
	s_nop 1
	v_cndmask_b32_e32 v3, v3, v6, vcc
	v_sub_u32_e32 v6, v5, v4
	v_cndmask_b32_e32 v5, v5, v6, vcc
	v_add_u32_e32 v6, 1, v3
	v_cmp_ge_u32_e32 vcc, v5, v4
	v_add_u32_e32 v5, 1, v7
	s_nop 0
	v_cndmask_b32_e32 v3, v3, v6, vcc
	v_mul_lo_u32 v6, v4, v3
	v_add_u32_e32 v4, v6, v4
	v_cmp_ne_u32_e32 vcc, v5, v4
	s_and_saveexec_b64 s[8:9], vcc
	s_xor_b64 s[8:9], exec, s[8:9]
	s_cbranch_execz .LBB0_1093
	s_waitcnt lgkmcnt(0)
	s_add_u32 s14, s34, 0x7500
	s_addc_u32 s15, s35, 0
	v_mov_b32_e32 v2, 0
	global_load_dword v2, v2, s[14:15] sc1
	s_waitcnt vmcnt(0)
	v_cmp_eq_u32_e32 vcc, v2, v3
	s_and_saveexec_b64 s[10:11], vcc
	s_cbranch_execz .LBB0_1092
	s_add_u32 s12, s34, 0x4200
	s_addc_u32 s13, s35, 0
	s_mov_b32 s2, 1
	s_mov_b64 s[18:19], 0
	s_branch .LBB0_1083

; __device__ __forceinline__ unsigned xb_ld(unsigned* p)              { return __hip_atomic_load(p, __ATOMIC_RELAXED, __HIP_MEMORY_SCOPE_AGENT); }
; __device__ __forceinline__ unsigned xb_add(unsigned* p, unsigned v) { return __hip_atomic_fetch_add(p, v, __ATOMIC_RELAXED, __HIP_MEMORY_SCOPE_AGENT); }
; #define XB_SPIN(cond, bar) do { unsigned _sp = 0; while (cond) { __builtin_amdgcn_s_sleep(1); \
;     if ((++_sp & 255u) == 0u) { if (xb_ld(&(bar)[XB_TMO])) break; if (_sp > XB_SPIN_CAP) { atomicAdd(&(bar)[XB_TMO], 1u); break; } } } } while (0)
; __device__ __forceinline__ void xcd_barrier(const XcdBarrier& b) {
;     ...
;         const unsigned old = xb_add(&bar[XB_XSUB(b.x)], 1u);
;         const unsigned gen = old / nloc;
;         if (old + 1u == (gen + 1u) * nloc) {
;             __builtin_amdgcn_fence(__ATOMIC_RELEASE, "agent");
;             asm volatile("s_waitcnt vmcnt(0)" ::: "memory");
;             const unsigned og = xb_add(&bar[XB_TOP], 1u);
;             const unsigned tg = og / nx;
;             if (og + 1u == (tg + 1u) * nx) xb_add(&bar[XB_TOPGEN], 1u);
;             else XB_SPIN(xb_ld(&bar[XB_TOPGEN]) == tg, bar);
;             __builtin_amdgcn_fence(__ATOMIC_ACQUIRE, "agent");
;             xb_add(&bar[XB_XGEN(b.x)], 1u);
;             asm volatile("s_waitcnt vmcnt(0)" ::: "memory");
;         } else {
;             XB_SPIN(xb_ld(&bar[XB_XGEN(b.x)]) == gen, bar);
;             __builtin_amdgcn_fence(__ATOMIC_ACQUIRE, "agent");
;             asm volatile("s_waitcnt vmcnt(0)" ::: "memory");
;         }
.LBB0_1152:
	s_or_b64 exec, exec, s[10:11]
	v_cvt_f32_u32_e32 v6, v4
	s_waitcnt vmcnt(0)
	v_readfirstlane_b32 s2, v5
	v_sub_u32_e32 v5, 0, v4
	v_rcp_iflag_f32_e32 v6, v6
	v_add_u32_e32 v7, s2, v3
	v_mul_f32_e32 v6, 0x4f7ffffe, v6
	v_cvt_u32_f32_e32 v6, v6
	v_mul_lo_u32 v3, v5, v6
	v_mul_hi_u32 v3, v6, v3
	v_add_u32_e32 v3, v6, v3
	v_mul_hi_u32 v3, v7, v3
	v_mul_lo_u32 v5, v3, v4
	v_sub_u32_e32 v5, v7, v5
	v_add_u32_e32 v6, 1, v3
	v_cmp_ge_u32_e32 vcc, v5, v4
	s_nop 1
	v_cndmask_b32_e32 v3, v3, v6, vcc
	v_sub_u32_e32 v6, v5, v4
	v_cndmask_b32_e32 v5, v5, v6, vcc
	v_add_u32_e32 v6, 1, v3
	v_cmp_ge_u32_e32 vcc, v5, v4
	v_add_u32_e32 v5, 1, v7
	s_nop 0
	v_cndmask_b32_e32 v3, v3, v6, vcc
	v_mul_lo_u32 v6, v4, v3
	v_add_u32_e32 v4, v6, v4
	v_cmp_ne_u32_e32 vcc, v5, v4
	s_and_saveexec_b64 s[8:9], vcc
	s_xor_b64 s[8:9], exec, s[8:9]
	s_cbranch_execz .LBB0_1166
	s_waitcnt lgkmcnt(0)
	s_add_u32 s14, s34, 0x7500
	s_addc_u32 s15, s35, 0
	v_mov_b32_e32 v2, 0
	global_load_dword v2, v2, s[14:15] sc1
	s_waitcnt vmcnt(0)
	v_cmp_eq_u32_e32 vcc, v2, v3
	s_and_saveexec_b64 s[10:11], vcc
	s_cbranch_execz .LBB0_1165
	s_add_u32 s12, s34, 0x4200
	s_addc_u32 s13, s35, 0
	s_mov_b32 s2, 1
	s_mov_b64 s[16:17], 0
	s_branch .LBB0_1156

; __device__ __forceinline__ unsigned xb_ld(unsigned* p)              { return __hip_atomic_load(p, __ATOMIC_RELAXED, __HIP_MEMORY_SCOPE_AGENT); }
; __device__ __forceinline__ unsigned xb_add(unsigned* p, unsigned v) { return __hip_atomic_fetch_add(p, v, __ATOMIC_RELAXED, __HIP_MEMORY_SCOPE_AGENT); }
; #define XB_SPIN(cond, bar) do { unsigned _sp = 0; while (cond) { __builtin_amdgcn_s_sleep(1); \
;     if ((++_sp & 255u) == 0u) { if (xb_ld(&(bar)[XB_TMO])) break; if (_sp > XB_SPIN_CAP) { atomicAdd(&(bar)[XB_TMO], 1u); break; } } } } while (0)
; __device__ __forceinline__ void xcd_barrier(const XcdBarrier& b) {
;     ...
;         const unsigned old = xb_add(&bar[XB_XSUB(b.x)], 1u);
;         const unsigned gen = old / nloc;
;         if (old + 1u == (gen + 1u) * nloc) {
;             __builtin_amdgcn_fence(__ATOMIC_RELEASE, "agent");
;             asm volatile("s_waitcnt vmcnt(0)" ::: "memory");
;             const unsigned og = xb_add(&bar[XB_TOP], 1u);
;             const unsigned tg = og / nx;
;             if (og + 1u == (tg + 1u) * nx) xb_add(&bar[XB_TOPGEN], 1u);
;             else XB_SPIN(xb_ld(&bar[XB_TOPGEN]) == tg, bar);
;             __builtin_amdgcn_fence(__ATOMIC_ACQUIRE, "agent");
;             xb_add(&bar[XB_XGEN(b.x)], 1u);
;             asm volatile("s_waitcnt vmcnt(0)" ::: "memory");
;         } else {
;             XB_SPIN(xb_ld(&bar[XB_XGEN(b.x)]) == gen, bar);
;             __builtin_amdgcn_fence(__ATOMIC_ACQUIRE, "agent");
;             asm volatile("s_waitcnt vmcnt(0)" ::: "memory");
;         }
.LBB0_1349:
	s_or_b64 exec, exec, s[10:11]
	v_cvt_f32_u32_e32 v5, v3
	s_waitcnt vmcnt(0)
	v_readfirstlane_b32 s3, v4
	v_sub_u32_e32 v4, 0, v3
	v_rcp_iflag_f32_e32 v5, v5
	v_add_u32_e32 v6, s3, v1
	v_mul_f32_e32 v5, 0x4f7ffffe, v5
	v_cvt_u32_f32_e32 v5, v5
	v_mul_lo_u32 v1, v4, v5
	v_mul_hi_u32 v1, v5, v1
	v_add_u32_e32 v1, v5, v1
	v_mul_hi_u32 v1, v6, v1
	v_mul_lo_u32 v4, v1, v3
	v_sub_u32_e32 v4, v6, v4
	v_add_u32_e32 v5, 1, v1
	v_cmp_ge_u32_e32 vcc, v4, v3
	s_nop 1
	v_cndmask_b32_e32 v1, v1, v5, vcc
	v_sub_u32_e32 v5, v4, v3
	v_cndmask_b32_e32 v4, v4, v5, vcc
	v_add_u32_e32 v5, 1, v1
	v_cmp_ge_u32_e32 vcc, v4, v3
	v_add_u32_e32 v4, 1, v6
	s_nop 0
	v_cndmask_b32_e32 v1, v1, v5, vcc
	v_mul_lo_u32 v5, v3, v1
	v_add_u32_e32 v3, v5, v3
	v_cmp_ne_u32_e32 vcc, v4, v3
	s_and_saveexec_b64 s[8:9], vcc
	s_xor_b64 s[8:9], exec, s[8:9]
	s_cbranch_execz .LBB0_1363
	s_waitcnt lgkmcnt(0)
	s_add_u32 s14, s34, 0x7500
	s_addc_u32 s15, s35, 0
	v_mov_b32_e32 v2, 0
	global_load_dword v2, v2, s[14:15] sc1
	s_waitcnt vmcnt(0)
	v_cmp_eq_u32_e32 vcc, v2, v1
	s_and_saveexec_b64 s[10:11], vcc
	s_cbranch_execz .LBB0_1362
	s_add_u32 s12, s34, 0x4200
	s_addc_u32 s13, s35, 0
	s_mov_b32 s3, 1
	s_mov_b64 s[16:17], 0
	s_branch .LBB0_1353

; __device__ __forceinline__ unsigned xb_ld(unsigned* p)              { return __hip_atomic_load(p, __ATOMIC_RELAXED, __HIP_MEMORY_SCOPE_AGENT); }
; __device__ __forceinline__ unsigned xb_add(unsigned* p, unsigned v) { return __hip_atomic_fetch_add(p, v, __ATOMIC_RELAXED, __HIP_MEMORY_SCOPE_AGENT); }
; #define XB_SPIN(cond, bar) do { unsigned _sp = 0; while (cond) { __builtin_amdgcn_s_sleep(1); \
;     if ((++_sp & 255u) == 0u) { if (xb_ld(&(bar)[XB_TMO])) break; if (_sp > XB_SPIN_CAP) { atomicAdd(&(bar)[XB_TMO], 1u); break; } } } } while (0)
; __device__ __forceinline__ void xcd_barrier(const XcdBarrier& b) {
;     ...
;         const unsigned old = xb_add(&bar[XB_XSUB(b.x)], 1u);
;         const unsigned gen = old / nloc;
;         if (old + 1u == (gen + 1u) * nloc) {
;             __builtin_amdgcn_fence(__ATOMIC_RELEASE, "agent");
;             asm volatile("s_waitcnt vmcnt(0)" ::: "memory");
;             const unsigned og = xb_add(&bar[XB_TOP], 1u);
;             const unsigned tg = og / nx;
;             if (og + 1u == (tg + 1u) * nx) xb_add(&bar[XB_TOPGEN], 1u);
;             else XB_SPIN(xb_ld(&bar[XB_TOPGEN]) == tg, bar);
;             __builtin_amdgcn_fence(__ATOMIC_ACQUIRE, "agent");
;             xb_add(&bar[XB_XGEN(b.x)], 1u);
;             asm volatile("s_waitcnt vmcnt(0)" ::: "memory");
;         } else {
;             XB_SPIN(xb_ld(&bar[XB_XGEN(b.x)]) == gen, bar);
;             __builtin_amdgcn_fence(__ATOMIC_ACQUIRE, "agent");
;             asm volatile("s_waitcnt vmcnt(0)" ::: "memory");
;         }
.LBB0_1427:
	s_or_b64 exec, exec, s[10:11]
	v_cvt_f32_u32_e32 v5, v3
	s_waitcnt vmcnt(0)
	v_readfirstlane_b32 s8, v4
	v_sub_u32_e32 v4, 0, v3
	v_rcp_iflag_f32_e32 v5, v5
	v_add_u32_e32 v6, s8, v1
	v_mul_f32_e32 v5, 0x4f7ffffe, v5
	v_cvt_u32_f32_e32 v5, v5
	v_mul_lo_u32 v1, v4, v5
	v_mul_hi_u32 v1, v5, v1
	v_add_u32_e32 v1, v5, v1
	v_mul_hi_u32 v1, v6, v1
	v_mul_lo_u32 v4, v1, v3
	v_sub_u32_e32 v4, v6, v4
	v_add_u32_e32 v5, 1, v1
	v_cmp_ge_u32_e32 vcc, v4, v3
	s_nop 1
	v_cndmask_b32_e32 v1, v1, v5, vcc
	v_sub_u32_e32 v5, v4, v3
	v_cndmask_b32_e32 v4, v4, v5, vcc
	v_add_u32_e32 v5, 1, v1
	v_cmp_ge_u32_e32 vcc, v4, v3
	v_add_u32_e32 v4, 1, v6
	s_nop 0
	v_cndmask_b32_e32 v1, v1, v5, vcc
	v_mul_lo_u32 v5, v3, v1
	v_add_u32_e32 v3, v5, v3
	v_cmp_ne_u32_e32 vcc, v4, v3
	s_and_saveexec_b64 s[8:9], vcc
	s_xor_b64 s[8:9], exec, s[8:9]
	s_cbranch_execz .LBB0_1441
	s_waitcnt lgkmcnt(0)
	s_add_u32 s14, s34, 0x7500
	s_addc_u32 s15, s35, 0
	v_mov_b32_e32 v2, 0
	global_load_dword v2, v2, s[14:15] sc1
	s_waitcnt vmcnt(0)
	v_cmp_eq_u32_e32 vcc, v2, v1
	s_and_saveexec_b64 s[10:11], vcc
	s_cbranch_execz .LBB0_1440
	s_add_u32 s12, s34, 0x4200
	s_addc_u32 s13, s35, 0
	s_mov_b32 s26, 1
	s_mov_b64 s[16:17], 0
	s_branch .LBB0_1431
